# lever 7 (instruction selection): the two per-element constant multiplies of the LoRA epilogue as v_pk_mul_f32 (same products)
# speedup vs baseline: 1.0033x; 1.0033x over previous
; __device__ __forceinline__ unsigned cvt_pk_bf16(float lo, float hi) { const f32x2c v = {lo, hi}; const bf16x2c b = __builtin_convertvector(v, bf16x2c); return __builtin_bit_cast(unsigned, b); }
; __device__ __forceinline__ float sigmoidf_(float x) { return 1.f / (1.f + __expf(-x)); }
;     __device__ __forceinline__ void operator()(const f32x4 (&acc)[2][2][4][2], const Unit& u, int wr, int wc, int fr, int fq) const {
;         const int row0 = u.pm * BM + wr * 64 + fr, col0 = u.pn * BM + wc * 32 + 8 * fq;
;         const int kind = u.pn >> 1;
;         bf16* O = LW + (size_t)kind * ostride;
; #pragma unroll
;         for (int bj = 0; bj < 2; ++bj) { const int col = (col0 + bj * HALF) & 511;
;             f32x4 b0 = (f32x4){0.f, 0.f, 0.f, 0.f}, b1 = b0;
;             if (kind == 0) { b0 = *(const f32x4*)(w0 + col); b1 = *(const f32x4*)(w0 + col + 4); }
;             else if (kind == 1) { b0 = *(const f32x4*)(a0 + col); b1 = *(const f32x4*)(a0 + col + 4); }
; #pragma unroll
;             for (int ai = 0; ai < 2; ++ai)
; #pragma unroll
;                 for (int m = 0; m < 4; ++m) { const size_t row = (size_t)(row0 + ai * HALF + m * 16);
;                     const f32x4 v0 = acc[ai][bj][m][0] + b0, v1 = acc[ai][bj][m][1] + b1; float o[8];
; #pragma unroll
;                     for (int e = 0; e < 8; ++e) { float x = (e < 4) ? v0[e & 3] : v1[e & 3];
;                         if (kind == 0) x = -0.6065306597126334f * sigmoidf_(x);
;                         else if (kind == 1) x = sigmoidf_(x);
;                         o[e] = x; }
;                     u32x4 w; w.x = cvt_pk_bf16(o[0], o[1]); w.y = cvt_pk_bf16(o[2], o[3]); w.z = cvt_pk_bf16(o[4], o[5]); w.w = cvt_pk_bf16(o[6], o[7]);
;                     *(u32x4*)(O + row * 512 + col) = w; } }
.LBB0_571:
	s_lshl_b32 s0, s33, 8
	s_ashr_i32 s76, s33, 1
	s_and_b32 s0, s0, 0x100
	v_or_b32_e32 v136, s0, v154
	s_ashr_i32 s77, s76, 31
	s_lshl_b64 s[2:3], s[76:77], 26
	s_add_u32 s2, s28, s2
	s_addc_u32 s3, s29, s3
	v_lshl_add_u32 v156, s68, 8, v152
	v_ashrrev_i32_e32 v157, 31, v156
	v_lshlrev_b64 v[156:157], 10, v[156:157]
	v_lshlrev_b32_e32 v158, 1, v136
	v_mov_b32_e32 v159, v137
	v_lshl_add_u64 v[156:157], v[156:157], 0, v[158:159]
	v_lshl_add_u64 v[156:157], s[2:3], 0, v[156:157]
	s_cmp_gt_u32 s33, 3
	s_cbranch_scc1 .Llora_g
	s_cmp_lt_u32 s33, 2
	s_cselect_b32 s5, s67, s71
	s_cselect_b32 s4, s66, s70
	v_lshlrev_b32_e32 v160, 2, v136
	s_nop 0
	global_load_dwordx4 v[164:167], v160, s[4:5]
	global_load_dwordx4 v[168:171], v160, s[4:5] offset:16
	global_load_dwordx4 v[172:175], v160, s[4:5] offset:512
	global_load_dwordx4 v[176:179], v160, s[4:5] offset:528
	s_cmp_lt_u32 s33, 2
	s_cselect_b32 s0, 0xbf1b4598, 1.0
	v_mov_b32_e32 v196, 0xbfb8aa3b
	v_mov_b32_e32 v197, 0xbfb8aa3b
	v_mov_b32_e32 v198, s0
	v_mov_b32_e32 v199, s0
	s_waitcnt vmcnt(0)
	v_pk_add_f32 v[132:133], v[132:133], v[164:165]
	v_pk_add_f32 v[134:135], v[134:135], v[166:167]
	v_pk_add_f32 v[128:129], v[128:129], v[168:169]
	v_pk_add_f32 v[130:131], v[130:131], v[170:171]
	v_pk_mul_f32 v[132:133], v[132:133], v[196:197]
	v_pk_mul_f32 v[134:135], v[134:135], v[196:197]
	v_pk_mul_f32 v[128:129], v[128:129], v[196:197]
	v_pk_mul_f32 v[130:131], v[130:131], v[196:197]
	v_exp_f32_e32 v132, v132
	v_exp_f32_e32 v133, v133
	v_exp_f32_e32 v134, v134
	v_exp_f32_e32 v135, v135
	v_exp_f32_e32 v128, v128
	v_exp_f32_e32 v129, v129
	v_exp_f32_e32 v130, v130
	v_exp_f32_e32 v131, v131
	v_pk_add_f32 v[132:133], v[132:133], 1.0 op_sel_hi:[1,0]
	v_pk_add_f32 v[134:135], v[134:135], 1.0 op_sel_hi:[1,0]
	v_pk_add_f32 v[128:129], v[128:129], 1.0 op_sel_hi:[1,0]
	v_pk_add_f32 v[130:131], v[130:131], 1.0 op_sel_hi:[1,0]
	v_div_scale_f32 v180, s[100:101], v132, v132, 1.0
	v_rcp_f32_e32 v181, v180
	v_div_scale_f32 v182, vcc, 1.0, v132, 1.0
	v_fma_f32 v183, -v180, v181, 1.0
	v_fmac_f32_e32 v181, v183, v181
	v_mul_f32_e32 v183, v182, v181
	v_fma_f32 v184, -v180, v183, v182
	v_fmac_f32_e32 v183, v184, v181
	v_fma_f32 v180, -v180, v183, v182
	v_div_fmas_f32 v180, v180, v181, v183
	v_div_fixup_f32 v132, v180, v132, 1.0
	v_div_scale_f32 v180, s[100:101], v133, v133, 1.0
	v_rcp_f32_e32 v181, v180
	v_div_scale_f32 v182, vcc, 1.0, v133, 1.0
	v_fma_f32 v183, -v180, v181, 1.0
	v_fmac_f32_e32 v181, v183, v181
	v_mul_f32_e32 v183, v182, v181
	v_fma_f32 v184, -v180, v183, v182
	v_fmac_f32_e32 v183, v184, v181
	v_fma_f32 v180, -v180, v183, v182
	v_div_fmas_f32 v180, v180, v181, v183
	v_div_fixup_f32 v133, v180, v133, 1.0
	v_div_scale_f32 v180, s[100:101], v134, v134, 1.0
	v_rcp_f32_e32 v181, v180
	v_div_scale_f32 v182, vcc, 1.0, v134, 1.0
	v_fma_f32 v183, -v180, v181, 1.0
	v_fmac_f32_e32 v181, v183, v181
	v_mul_f32_e32 v183, v182, v181
	v_fma_f32 v184, -v180, v183, v182
	v_fmac_f32_e32 v183, v184, v181
	v_fma_f32 v180, -v180, v183, v182
	v_div_fmas_f32 v180, v180, v181, v183
	v_div_fixup_f32 v134, v180, v134, 1.0
	v_div_scale_f32 v180, s[100:101], v135, v135, 1.0
	v_rcp_f32_e32 v181, v180
	v_div_scale_f32 v182, vcc, 1.0, v135, 1.0
	v_fma_f32 v183, -v180, v181, 1.0
	v_fmac_f32_e32 v181, v183, v181
	v_mul_f32_e32 v183, v182, v181
	v_fma_f32 v184, -v180, v183, v182
	v_fmac_f32_e32 v183, v184, v181
	v_fma_f32 v180, -v180, v183, v182
	v_div_fmas_f32 v180, v180, v181, v183
	v_div_fixup_f32 v135, v180, v135, 1.0
	v_div_scale_f32 v180, s[100:101], v128, v128, 1.0
	v_rcp_f32_e32 v181, v180
	v_div_scale_f32 v182, vcc, 1.0, v128, 1.0
	v_fma_f32 v183, -v180, v181, 1.0
	v_fmac_f32_e32 v181, v183, v181
	v_mul_f32_e32 v183, v182, v181
	v_fma_f32 v184, -v180, v183, v182
	v_fmac_f32_e32 v183, v184, v181
	v_fma_f32 v180, -v180, v183, v182
	v_div_fmas_f32 v180, v180, v181, v183
	v_div_fixup_f32 v128, v180, v128, 1.0
	v_div_scale_f32 v180, s[100:101], v129, v129, 1.0
	v_rcp_f32_e32 v181, v180
	v_div_scale_f32 v182, vcc, 1.0, v129, 1.0
	v_fma_f32 v183, -v180, v181, 1.0
	v_fmac_f32_e32 v181, v183, v181
	v_mul_f32_e32 v183, v182, v181
	v_fma_f32 v184, -v180, v183, v182
	v_fmac_f32_e32 v183, v184, v181
	v_fma_f32 v180, -v180, v183, v182
	v_div_fmas_f32 v180, v180, v181, v183
	v_div_fixup_f32 v129, v180, v129, 1.0
	v_div_scale_f32 v180, s[100:101], v130, v130, 1.0
	v_rcp_f32_e32 v181, v180
	v_div_scale_f32 v182, vcc, 1.0, v130, 1.0
	v_fma_f32 v183, -v180, v181, 1.0
	v_fmac_f32_e32 v181, v183, v181
	v_mul_f32_e32 v183, v182, v181
	v_fma_f32 v184, -v180, v183, v182
	v_fmac_f32_e32 v183, v184, v181
	v_fma_f32 v180, -v180, v183, v182
	v_div_fmas_f32 v180, v180, v181, v183
	v_div_fixup_f32 v130, v180, v130, 1.0
	v_div_scale_f32 v180, s[100:101], v131, v131, 1.0
	v_rcp_f32_e32 v181, v180
	v_div_scale_f32 v182, vcc, 1.0, v131, 1.0
	v_fma_f32 v183, -v180, v181, 1.0
	v_fmac_f32_e32 v181, v183, v181
	v_mul_f32_e32 v183, v182, v181
	v_fma_f32 v184, -v180, v183, v182
	v_fmac_f32_e32 v183, v184, v181
	v_fma_f32 v180, -v180, v183, v182
	v_div_fmas_f32 v180, v180, v181, v183
	v_div_fixup_f32 v131, v180, v131, 1.0
	v_pk_mul_f32 v[132:133], v[132:133], v[198:199]
	v_pk_mul_f32 v[134:135], v[134:135], v[198:199]
	v_pk_mul_f32 v[128:129], v[128:129], v[198:199]
	v_pk_mul_f32 v[130:131], v[130:131], v[198:199]
	v_cvt_pk_bf16_f32 v188, v132, v133
	v_cvt_pk_bf16_f32 v189, v134, v135
	v_cvt_pk_bf16_f32 v190, v128, v129
	v_cvt_pk_bf16_f32 v191, v130, v131
	global_store_dwordx4 v[156:157], v[188:191], off
	v_pk_add_f32 v[124:125], v[124:125], v[164:165]
	v_pk_add_f32 v[126:127], v[126:127], v[166:167]
	v_pk_add_f32 v[120:121], v[120:121], v[168:169]
; __device__ __forceinline__ unsigned cvt_pk_bf16(float lo, float hi) { const f32x2c v = {lo, hi}; const bf16x2c b = __builtin_convertvector(v, bf16x2c); return __builtin_bit_cast(unsigned, b); }
; __device__ __forceinline__ float sigmoidf_(float x) { return 1.f / (1.f + __expf(-x)); }
;     __device__ __forceinline__ void operator()(const f32x4 (&acc)[2][2][4][2], const Unit& u, int wr, int wc, int fr, int fq) const {
;     ...
;                     const f32x4 v0 = acc[ai][bj][m][0] + b0, v1 = acc[ai][bj][m][1] + b1; float o[8];
; #pragma unroll
;                     for (int e = 0; e < 8; ++e) { float x = (e < 4) ? v0[e & 3] : v1[e & 3];
;                         if (kind == 0) x = -0.6065306597126334f * sigmoidf_(x);
;                         else if (kind == 1) x = sigmoidf_(x);
;                         o[e] = x; }
;                     u32x4 w; w.x = cvt_pk_bf16(o[0], o[1]); w.y = cvt_pk_bf16(o[2], o[3]); w.z = cvt_pk_bf16(o[4], o[5]); w.w = cvt_pk_bf16(o[6], o[7]);
;                     *(u32x4*)(O + row * 512 + col) = w; } }
	v_pk_add_f32 v[122:123], v[122:123], v[170:171]
	v_pk_mul_f32 v[124:125], v[124:125], v[196:197]
	v_pk_mul_f32 v[126:127], v[126:127], v[196:197]
	v_pk_mul_f32 v[120:121], v[120:121], v[196:197]
	v_pk_mul_f32 v[122:123], v[122:123], v[196:197]
	v_exp_f32_e32 v124, v124
	v_exp_f32_e32 v125, v125
	v_exp_f32_e32 v126, v126
	v_exp_f32_e32 v127, v127
	v_exp_f32_e32 v120, v120
	v_exp_f32_e32 v121, v121
	v_exp_f32_e32 v122, v122
	v_exp_f32_e32 v123, v123
	v_pk_add_f32 v[124:125], v[124:125], 1.0 op_sel_hi:[1,0]
	v_pk_add_f32 v[126:127], v[126:127], 1.0 op_sel_hi:[1,0]
	v_pk_add_f32 v[120:121], v[120:121], 1.0 op_sel_hi:[1,0]
	v_pk_add_f32 v[122:123], v[122:123], 1.0 op_sel_hi:[1,0]
	v_div_scale_f32 v180, s[100:101], v124, v124, 1.0
	v_rcp_f32_e32 v181, v180
	v_div_scale_f32 v182, vcc, 1.0, v124, 1.0
	v_fma_f32 v183, -v180, v181, 1.0
	v_fmac_f32_e32 v181, v183, v181
	v_mul_f32_e32 v183, v182, v181
	v_fma_f32 v184, -v180, v183, v182
	v_fmac_f32_e32 v183, v184, v181
	v_fma_f32 v180, -v180, v183, v182
	v_div_fmas_f32 v180, v180, v181, v183
	v_div_fixup_f32 v124, v180, v124, 1.0
	v_div_scale_f32 v180, s[100:101], v125, v125, 1.0
	v_rcp_f32_e32 v181, v180
	v_div_scale_f32 v182, vcc, 1.0, v125, 1.0
	v_fma_f32 v183, -v180, v181, 1.0
	v_fmac_f32_e32 v181, v183, v181
	v_mul_f32_e32 v183, v182, v181
	v_fma_f32 v184, -v180, v183, v182
	v_fmac_f32_e32 v183, v184, v181
	v_fma_f32 v180, -v180, v183, v182
	v_div_fmas_f32 v180, v180, v181, v183
	v_div_fixup_f32 v125, v180, v125, 1.0
	v_div_scale_f32 v180, s[100:101], v126, v126, 1.0
	v_rcp_f32_e32 v181, v180
	v_div_scale_f32 v182, vcc, 1.0, v126, 1.0
	v_fma_f32 v183, -v180, v181, 1.0
	v_fmac_f32_e32 v181, v183, v181
	v_mul_f32_e32 v183, v182, v181
	v_fma_f32 v184, -v180, v183, v182
	v_fmac_f32_e32 v183, v184, v181
	v_fma_f32 v180, -v180, v183, v182
	v_div_fmas_f32 v180, v180, v181, v183
	v_div_fixup_f32 v126, v180, v126, 1.0
	v_div_scale_f32 v180, s[100:101], v127, v127, 1.0
	v_rcp_f32_e32 v181, v180
	v_div_scale_f32 v182, vcc, 1.0, v127, 1.0
	v_fma_f32 v183, -v180, v181, 1.0
	v_fmac_f32_e32 v181, v183, v181
	v_mul_f32_e32 v183, v182, v181
	v_fma_f32 v184, -v180, v183, v182
	v_fmac_f32_e32 v183, v184, v181
	v_fma_f32 v180, -v180, v183, v182
	v_div_fmas_f32 v180, v180, v181, v183
	v_div_fixup_f32 v127, v180, v127, 1.0
	v_div_scale_f32 v180, s[100:101], v120, v120, 1.0
	v_rcp_f32_e32 v181, v180
	v_div_scale_f32 v182, vcc, 1.0, v120, 1.0
	v_fma_f32 v183, -v180, v181, 1.0
	v_fmac_f32_e32 v181, v183, v181
	v_mul_f32_e32 v183, v182, v181
	v_fma_f32 v184, -v180, v183, v182
	v_fmac_f32_e32 v183, v184, v181
	v_fma_f32 v180, -v180, v183, v182
	v_div_fmas_f32 v180, v180, v181, v183
	v_div_fixup_f32 v120, v180, v120, 1.0
	v_div_scale_f32 v180, s[100:101], v121, v121, 1.0
	v_rcp_f32_e32 v181, v180
	v_div_scale_f32 v182, vcc, 1.0, v121, 1.0
	v_fma_f32 v183, -v180, v181, 1.0
	v_fmac_f32_e32 v181, v183, v181
	v_mul_f32_e32 v183, v182, v181
	v_fma_f32 v184, -v180, v183, v182
	v_fmac_f32_e32 v183, v184, v181
	v_fma_f32 v180, -v180, v183, v182
	v_div_fmas_f32 v180, v180, v181, v183
	v_div_fixup_f32 v121, v180, v121, 1.0
	v_div_scale_f32 v180, s[100:101], v122, v122, 1.0
	v_rcp_f32_e32 v181, v180
	v_div_scale_f32 v182, vcc, 1.0, v122, 1.0
	v_fma_f32 v183, -v180, v181, 1.0
	v_fmac_f32_e32 v181, v183, v181
	v_mul_f32_e32 v183, v182, v181
	v_fma_f32 v184, -v180, v183, v182
	v_fmac_f32_e32 v183, v184, v181
	v_fma_f32 v180, -v180, v183, v182
	v_div_fmas_f32 v180, v180, v181, v183
	v_div_fixup_f32 v122, v180, v122, 1.0
	v_div_scale_f32 v180, s[100:101], v123, v123, 1.0
	v_rcp_f32_e32 v181, v180
	v_div_scale_f32 v182, vcc, 1.0, v123, 1.0
	v_fma_f32 v183, -v180, v181, 1.0
	v_fmac_f32_e32 v181, v183, v181
	v_mul_f32_e32 v183, v182, v181
	v_fma_f32 v184, -v180, v183, v182
	v_fmac_f32_e32 v183, v184, v181
	v_fma_f32 v180, -v180, v183, v182
	v_div_fmas_f32 v180, v180, v181, v183
	v_div_fixup_f32 v123, v180, v123, 1.0
	v_pk_mul_f32 v[124:125], v[124:125], v[198:199]
	v_pk_mul_f32 v[126:127], v[126:127], v[198:199]
	v_pk_mul_f32 v[120:121], v[120:121], v[198:199]
	v_pk_mul_f32 v[122:123], v[122:123], v[198:199]
	s_mov_b64 s[98:99], 0x4000
	v_lshl_add_u64 v[158:159], v[156:157], 0, s[98:99]
	v_cvt_pk_bf16_f32 v192, v124, v125
	v_cvt_pk_bf16_f32 v193, v126, v127
	v_cvt_pk_bf16_f32 v194, v120, v121
	v_cvt_pk_bf16_f32 v195, v122, v123
	global_store_dwordx4 v[158:159], v[192:195], off
	v_pk_add_f32 v[116:117], v[116:117], v[164:165]
	v_pk_add_f32 v[118:119], v[118:119], v[166:167]
	v_pk_add_f32 v[112:113], v[112:113], v[168:169]
	v_pk_add_f32 v[114:115], v[114:115], v[170:171]
	v_pk_mul_f32 v[116:117], v[116:117], v[196:197]
	v_pk_mul_f32 v[118:119], v[118:119], v[196:197]
	v_pk_mul_f32 v[112:113], v[112:113], v[196:197]
	v_pk_mul_f32 v[114:115], v[114:115], v[196:197]
	v_exp_f32_e32 v116, v116
	v_exp_f32_e32 v117, v117
	v_exp_f32_e32 v118, v118
	v_exp_f32_e32 v119, v119
	v_exp_f32_e32 v112, v112
	v_exp_f32_e32 v113, v113
	v_exp_f32_e32 v114, v114
	v_exp_f32_e32 v115, v115
	v_pk_add_f32 v[116:117], v[116:117], 1.0 op_sel_hi:[1,0]
	v_pk_add_f32 v[118:119], v[118:119], 1.0 op_sel_hi:[1,0]
	v_pk_add_f32 v[112:113], v[112:113], 1.0 op_sel_hi:[1,0]
	v_pk_add_f32 v[114:115], v[114:115], 1.0 op_sel_hi:[1,0]
	v_div_scale_f32 v180, s[100:101], v116, v116, 1.0
	v_rcp_f32_e32 v181, v180
	v_div_scale_f32 v182, vcc, 1.0, v116, 1.0
	v_fma_f32 v183, -v180, v181, 1.0
	v_fmac_f32_e32 v181, v183, v181
	v_mul_f32_e32 v183, v182, v181
	v_fma_f32 v184, -v180, v183, v182
	v_fmac_f32_e32 v183, v184, v181
	v_fma_f32 v180, -v180, v183, v182
	v_div_fmas_f32 v180, v180, v181, v183
	v_div_fixup_f32 v116, v180, v116, 1.0
	v_div_scale_f32 v180, s[100:101], v117, v117, 1.0
; __device__ __forceinline__ unsigned cvt_pk_bf16(float lo, float hi) { const f32x2c v = {lo, hi}; const bf16x2c b = __builtin_convertvector(v, bf16x2c); return __builtin_bit_cast(unsigned, b); }
; __device__ __forceinline__ float sigmoidf_(float x) { return 1.f / (1.f + __expf(-x)); }
;     __device__ __forceinline__ void operator()(const f32x4 (&acc)[2][2][4][2], const Unit& u, int wr, int wc, int fr, int fq) const {
;     ...
;                     const f32x4 v0 = acc[ai][bj][m][0] + b0, v1 = acc[ai][bj][m][1] + b1; float o[8];
; #pragma unroll
;                     for (int e = 0; e < 8; ++e) { float x = (e < 4) ? v0[e & 3] : v1[e & 3];
;                         if (kind == 0) x = -0.6065306597126334f * sigmoidf_(x);
;                         else if (kind == 1) x = sigmoidf_(x);
;                         o[e] = x; }
;                     u32x4 w; w.x = cvt_pk_bf16(o[0], o[1]); w.y = cvt_pk_bf16(o[2], o[3]); w.z = cvt_pk_bf16(o[4], o[5]); w.w = cvt_pk_bf16(o[6], o[7]);
;                     *(u32x4*)(O + row * 512 + col) = w; } }
	v_rcp_f32_e32 v181, v180
	v_div_scale_f32 v182, vcc, 1.0, v117, 1.0
	v_fma_f32 v183, -v180, v181, 1.0
	v_fmac_f32_e32 v181, v183, v181
	v_mul_f32_e32 v183, v182, v181
	v_fma_f32 v184, -v180, v183, v182
	v_fmac_f32_e32 v183, v184, v181
	v_fma_f32 v180, -v180, v183, v182
	v_div_fmas_f32 v180, v180, v181, v183
	v_div_fixup_f32 v117, v180, v117, 1.0
	v_div_scale_f32 v180, s[100:101], v118, v118, 1.0
	v_rcp_f32_e32 v181, v180
	v_div_scale_f32 v182, vcc, 1.0, v118, 1.0
	v_fma_f32 v183, -v180, v181, 1.0
	v_fmac_f32_e32 v181, v183, v181
	v_mul_f32_e32 v183, v182, v181
	v_fma_f32 v184, -v180, v183, v182
	v_fmac_f32_e32 v183, v184, v181
	v_fma_f32 v180, -v180, v183, v182
	v_div_fmas_f32 v180, v180, v181, v183
	v_div_fixup_f32 v118, v180, v118, 1.0
	v_div_scale_f32 v180, s[100:101], v119, v119, 1.0
	v_rcp_f32_e32 v181, v180
	v_div_scale_f32 v182, vcc, 1.0, v119, 1.0
	v_fma_f32 v183, -v180, v181, 1.0
	v_fmac_f32_e32 v181, v183, v181
	v_mul_f32_e32 v183, v182, v181
	v_fma_f32 v184, -v180, v183, v182
	v_fmac_f32_e32 v183, v184, v181
	v_fma_f32 v180, -v180, v183, v182
	v_div_fmas_f32 v180, v180, v181, v183
	v_div_fixup_f32 v119, v180, v119, 1.0
	v_div_scale_f32 v180, s[100:101], v112, v112, 1.0
	v_rcp_f32_e32 v181, v180
	v_div_scale_f32 v182, vcc, 1.0, v112, 1.0
	v_fma_f32 v183, -v180, v181, 1.0
	v_fmac_f32_e32 v181, v183, v181
	v_mul_f32_e32 v183, v182, v181
	v_fma_f32 v184, -v180, v183, v182
	v_fmac_f32_e32 v183, v184, v181
	v_fma_f32 v180, -v180, v183, v182
	v_div_fmas_f32 v180, v180, v181, v183
	v_div_fixup_f32 v112, v180, v112, 1.0
	v_div_scale_f32 v180, s[100:101], v113, v113, 1.0
	v_rcp_f32_e32 v181, v180
	v_div_scale_f32 v182, vcc, 1.0, v113, 1.0
	v_fma_f32 v183, -v180, v181, 1.0
	v_fmac_f32_e32 v181, v183, v181
	v_mul_f32_e32 v183, v182, v181
	v_fma_f32 v184, -v180, v183, v182
	v_fmac_f32_e32 v183, v184, v181
	v_fma_f32 v180, -v180, v183, v182
	v_div_fmas_f32 v180, v180, v181, v183
	v_div_fixup_f32 v113, v180, v113, 1.0
	v_div_scale_f32 v180, s[100:101], v114, v114, 1.0
	v_rcp_f32_e32 v181, v180
	v_div_scale_f32 v182, vcc, 1.0, v114, 1.0
	v_fma_f32 v183, -v180, v181, 1.0
	v_fmac_f32_e32 v181, v183, v181
	v_mul_f32_e32 v183, v182, v181
	v_fma_f32 v184, -v180, v183, v182
	v_fmac_f32_e32 v183, v184, v181
	v_fma_f32 v180, -v180, v183, v182
	v_div_fmas_f32 v180, v180, v181, v183
	v_div_fixup_f32 v114, v180, v114, 1.0
	v_div_scale_f32 v180, s[100:101], v115, v115, 1.0
	v_rcp_f32_e32 v181, v180
	v_div_scale_f32 v182, vcc, 1.0, v115, 1.0
	v_fma_f32 v183, -v180, v181, 1.0
	v_fmac_f32_e32 v181, v183, v181
	v_mul_f32_e32 v183, v182, v181
	v_fma_f32 v184, -v180, v183, v182
	v_fmac_f32_e32 v183, v184, v181
	v_fma_f32 v180, -v180, v183, v182
	v_div_fmas_f32 v180, v180, v181, v183
	v_div_fixup_f32 v115, v180, v115, 1.0
	v_pk_mul_f32 v[116:117], v[116:117], v[198:199]
	v_pk_mul_f32 v[118:119], v[118:119], v[198:199]
	v_pk_mul_f32 v[112:113], v[112:113], v[198:199]
	v_pk_mul_f32 v[114:115], v[114:115], v[198:199]
	s_mov_b64 s[98:99], 0x8000
	v_lshl_add_u64 v[158:159], v[156:157], 0, s[98:99]
	v_cvt_pk_bf16_f32 v188, v116, v117
	v_cvt_pk_bf16_f32 v189, v118, v119
	v_cvt_pk_bf16_f32 v190, v112, v113
	v_cvt_pk_bf16_f32 v191, v114, v115
	global_store_dwordx4 v[158:159], v[188:191], off
	v_pk_add_f32 v[108:109], v[108:109], v[164:165]
	v_pk_add_f32 v[110:111], v[110:111], v[166:167]
	v_pk_add_f32 v[104:105], v[104:105], v[168:169]
	v_pk_add_f32 v[106:107], v[106:107], v[170:171]
	v_pk_mul_f32 v[108:109], v[108:109], v[196:197]
	v_pk_mul_f32 v[110:111], v[110:111], v[196:197]
	v_pk_mul_f32 v[104:105], v[104:105], v[196:197]
	v_pk_mul_f32 v[106:107], v[106:107], v[196:197]
	v_exp_f32_e32 v108, v108
	v_exp_f32_e32 v109, v109
	v_exp_f32_e32 v110, v110
	v_exp_f32_e32 v111, v111
	v_exp_f32_e32 v104, v104
	v_exp_f32_e32 v105, v105
	v_exp_f32_e32 v106, v106
	v_exp_f32_e32 v107, v107
	v_pk_add_f32 v[108:109], v[108:109], 1.0 op_sel_hi:[1,0]
	v_pk_add_f32 v[110:111], v[110:111], 1.0 op_sel_hi:[1,0]
	v_pk_add_f32 v[104:105], v[104:105], 1.0 op_sel_hi:[1,0]
	v_pk_add_f32 v[106:107], v[106:107], 1.0 op_sel_hi:[1,0]
	v_div_scale_f32 v180, s[100:101], v108, v108, 1.0
	v_rcp_f32_e32 v181, v180
	v_div_scale_f32 v182, vcc, 1.0, v108, 1.0
	v_fma_f32 v183, -v180, v181, 1.0
	v_fmac_f32_e32 v181, v183, v181
	v_mul_f32_e32 v183, v182, v181
	v_fma_f32 v184, -v180, v183, v182
	v_fmac_f32_e32 v183, v184, v181
	v_fma_f32 v180, -v180, v183, v182
	v_div_fmas_f32 v180, v180, v181, v183
	v_div_fixup_f32 v108, v180, v108, 1.0
	v_div_scale_f32 v180, s[100:101], v109, v109, 1.0
	v_rcp_f32_e32 v181, v180
	v_div_scale_f32 v182, vcc, 1.0, v109, 1.0
	v_fma_f32 v183, -v180, v181, 1.0
	v_fmac_f32_e32 v181, v183, v181
	v_mul_f32_e32 v183, v182, v181
	v_fma_f32 v184, -v180, v183, v182
	v_fmac_f32_e32 v183, v184, v181
	v_fma_f32 v180, -v180, v183, v182
	v_div_fmas_f32 v180, v180, v181, v183
	v_div_fixup_f32 v109, v180, v109, 1.0
	v_div_scale_f32 v180, s[100:101], v110, v110, 1.0
	v_rcp_f32_e32 v181, v180
	v_div_scale_f32 v182, vcc, 1.0, v110, 1.0
	v_fma_f32 v183, -v180, v181, 1.0
	v_fmac_f32_e32 v181, v183, v181
	v_mul_f32_e32 v183, v182, v181
	v_fma_f32 v184, -v180, v183, v182
	v_fmac_f32_e32 v183, v184, v181
	v_fma_f32 v180, -v180, v183, v182
	v_div_fmas_f32 v180, v180, v181, v183
	v_div_fixup_f32 v110, v180, v110, 1.0
	v_div_scale_f32 v180, s[100:101], v111, v111, 1.0
	v_rcp_f32_e32 v181, v180
	v_div_scale_f32 v182, vcc, 1.0, v111, 1.0
	v_fma_f32 v183, -v180, v181, 1.0
	v_fmac_f32_e32 v181, v183, v181
	v_mul_f32_e32 v183, v182, v181
	v_fma_f32 v184, -v180, v183, v182
	v_fmac_f32_e32 v183, v184, v181
	v_fma_f32 v180, -v180, v183, v182
	v_div_fmas_f32 v180, v180, v181, v183
	v_div_fixup_f32 v111, v180, v111, 1.0
; __device__ __forceinline__ unsigned cvt_pk_bf16(float lo, float hi) { const f32x2c v = {lo, hi}; const bf16x2c b = __builtin_convertvector(v, bf16x2c); return __builtin_bit_cast(unsigned, b); }
; __device__ __forceinline__ float sigmoidf_(float x) { return 1.f / (1.f + __expf(-x)); }
;     __device__ __forceinline__ void operator()(const f32x4 (&acc)[2][2][4][2], const Unit& u, int wr, int wc, int fr, int fq) const {
;     ...
;                     const f32x4 v0 = acc[ai][bj][m][0] + b0, v1 = acc[ai][bj][m][1] + b1; float o[8];
; #pragma unroll
;                     for (int e = 0; e < 8; ++e) { float x = (e < 4) ? v0[e & 3] : v1[e & 3];
;                         if (kind == 0) x = -0.6065306597126334f * sigmoidf_(x);
;                         else if (kind == 1) x = sigmoidf_(x);
;                         o[e] = x; }
;                     u32x4 w; w.x = cvt_pk_bf16(o[0], o[1]); w.y = cvt_pk_bf16(o[2], o[3]); w.z = cvt_pk_bf16(o[4], o[5]); w.w = cvt_pk_bf16(o[6], o[7]);
;                     *(u32x4*)(O + row * 512 + col) = w; } }
	v_div_scale_f32 v180, s[100:101], v104, v104, 1.0
	v_rcp_f32_e32 v181, v180
	v_div_scale_f32 v182, vcc, 1.0, v104, 1.0
	v_fma_f32 v183, -v180, v181, 1.0
	v_fmac_f32_e32 v181, v183, v181
	v_mul_f32_e32 v183, v182, v181
	v_fma_f32 v184, -v180, v183, v182
	v_fmac_f32_e32 v183, v184, v181
	v_fma_f32 v180, -v180, v183, v182
	v_div_fmas_f32 v180, v180, v181, v183
	v_div_fixup_f32 v104, v180, v104, 1.0
	v_div_scale_f32 v180, s[100:101], v105, v105, 1.0
	v_rcp_f32_e32 v181, v180
	v_div_scale_f32 v182, vcc, 1.0, v105, 1.0
	v_fma_f32 v183, -v180, v181, 1.0
	v_fmac_f32_e32 v181, v183, v181
	v_mul_f32_e32 v183, v182, v181
	v_fma_f32 v184, -v180, v183, v182
	v_fmac_f32_e32 v183, v184, v181
	v_fma_f32 v180, -v180, v183, v182
	v_div_fmas_f32 v180, v180, v181, v183
	v_div_fixup_f32 v105, v180, v105, 1.0
	v_div_scale_f32 v180, s[100:101], v106, v106, 1.0
	v_rcp_f32_e32 v181, v180
	v_div_scale_f32 v182, vcc, 1.0, v106, 1.0
	v_fma_f32 v183, -v180, v181, 1.0
	v_fmac_f32_e32 v181, v183, v181
	v_mul_f32_e32 v183, v182, v181
	v_fma_f32 v184, -v180, v183, v182
	v_fmac_f32_e32 v183, v184, v181
	v_fma_f32 v180, -v180, v183, v182
	v_div_fmas_f32 v180, v180, v181, v183
	v_div_fixup_f32 v106, v180, v106, 1.0
	v_div_scale_f32 v180, s[100:101], v107, v107, 1.0
	v_rcp_f32_e32 v181, v180
	v_div_scale_f32 v182, vcc, 1.0, v107, 1.0
	v_fma_f32 v183, -v180, v181, 1.0
	v_fmac_f32_e32 v181, v183, v181
	v_mul_f32_e32 v183, v182, v181
	v_fma_f32 v184, -v180, v183, v182
	v_fmac_f32_e32 v183, v184, v181
	v_fma_f32 v180, -v180, v183, v182
	v_div_fmas_f32 v180, v180, v181, v183
	v_div_fixup_f32 v107, v180, v107, 1.0
	v_pk_mul_f32 v[108:109], v[108:109], v[198:199]
	v_pk_mul_f32 v[110:111], v[110:111], v[198:199]
	v_pk_mul_f32 v[104:105], v[104:105], v[198:199]
	v_pk_mul_f32 v[106:107], v[106:107], v[198:199]
	s_mov_b64 s[98:99], 0xc000
	v_lshl_add_u64 v[158:159], v[156:157], 0, s[98:99]
	v_cvt_pk_bf16_f32 v192, v108, v109
	v_cvt_pk_bf16_f32 v193, v110, v111
	v_cvt_pk_bf16_f32 v194, v104, v105
	v_cvt_pk_bf16_f32 v195, v106, v107
	global_store_dwordx4 v[158:159], v[192:195], off
	v_pk_add_f32 v[100:101], v[100:101], v[164:165]
	v_pk_add_f32 v[102:103], v[102:103], v[166:167]
	v_pk_add_f32 v[96:97], v[96:97], v[168:169]
	v_pk_add_f32 v[98:99], v[98:99], v[170:171]
	v_pk_mul_f32 v[100:101], v[100:101], v[196:197]
	v_pk_mul_f32 v[102:103], v[102:103], v[196:197]
	v_pk_mul_f32 v[96:97], v[96:97], v[196:197]
	v_pk_mul_f32 v[98:99], v[98:99], v[196:197]
	v_exp_f32_e32 v100, v100
	v_exp_f32_e32 v101, v101
	v_exp_f32_e32 v102, v102
	v_exp_f32_e32 v103, v103
	v_exp_f32_e32 v96, v96
	v_exp_f32_e32 v97, v97
	v_exp_f32_e32 v98, v98
	v_exp_f32_e32 v99, v99
	v_pk_add_f32 v[100:101], v[100:101], 1.0 op_sel_hi:[1,0]
	v_pk_add_f32 v[102:103], v[102:103], 1.0 op_sel_hi:[1,0]
	v_pk_add_f32 v[96:97], v[96:97], 1.0 op_sel_hi:[1,0]
	v_pk_add_f32 v[98:99], v[98:99], 1.0 op_sel_hi:[1,0]
	v_div_scale_f32 v180, s[100:101], v100, v100, 1.0
	v_rcp_f32_e32 v181, v180
	v_div_scale_f32 v182, vcc, 1.0, v100, 1.0
	v_fma_f32 v183, -v180, v181, 1.0
	v_fmac_f32_e32 v181, v183, v181
	v_mul_f32_e32 v183, v182, v181
	v_fma_f32 v184, -v180, v183, v182
	v_fmac_f32_e32 v183, v184, v181
	v_fma_f32 v180, -v180, v183, v182
	v_div_fmas_f32 v180, v180, v181, v183
	v_div_fixup_f32 v100, v180, v100, 1.0
	v_div_scale_f32 v180, s[100:101], v101, v101, 1.0
	v_rcp_f32_e32 v181, v180
	v_div_scale_f32 v182, vcc, 1.0, v101, 1.0
	v_fma_f32 v183, -v180, v181, 1.0
	v_fmac_f32_e32 v181, v183, v181
	v_mul_f32_e32 v183, v182, v181
	v_fma_f32 v184, -v180, v183, v182
	v_fmac_f32_e32 v183, v184, v181
	v_fma_f32 v180, -v180, v183, v182
	v_div_fmas_f32 v180, v180, v181, v183
	v_div_fixup_f32 v101, v180, v101, 1.0
	v_div_scale_f32 v180, s[100:101], v102, v102, 1.0
	v_rcp_f32_e32 v181, v180
	v_div_scale_f32 v182, vcc, 1.0, v102, 1.0
	v_fma_f32 v183, -v180, v181, 1.0
	v_fmac_f32_e32 v181, v183, v181
	v_mul_f32_e32 v183, v182, v181
	v_fma_f32 v184, -v180, v183, v182
	v_fmac_f32_e32 v183, v184, v181
	v_fma_f32 v180, -v180, v183, v182
	v_div_fmas_f32 v180, v180, v181, v183
	v_div_fixup_f32 v102, v180, v102, 1.0
	v_div_scale_f32 v180, s[100:101], v103, v103, 1.0
	v_rcp_f32_e32 v181, v180
	v_div_scale_f32 v182, vcc, 1.0, v103, 1.0
	v_fma_f32 v183, -v180, v181, 1.0
	v_fmac_f32_e32 v181, v183, v181
	v_mul_f32_e32 v183, v182, v181
	v_fma_f32 v184, -v180, v183, v182
	v_fmac_f32_e32 v183, v184, v181
	v_fma_f32 v180, -v180, v183, v182
	v_div_fmas_f32 v180, v180, v181, v183
	v_div_fixup_f32 v103, v180, v103, 1.0
	v_div_scale_f32 v180, s[100:101], v96, v96, 1.0
	v_rcp_f32_e32 v181, v180
	v_div_scale_f32 v182, vcc, 1.0, v96, 1.0
	v_fma_f32 v183, -v180, v181, 1.0
	v_fmac_f32_e32 v181, v183, v181
	v_mul_f32_e32 v183, v182, v181
	v_fma_f32 v184, -v180, v183, v182
	v_fmac_f32_e32 v183, v184, v181
	v_fma_f32 v180, -v180, v183, v182
	v_div_fmas_f32 v180, v180, v181, v183
	v_div_fixup_f32 v96, v180, v96, 1.0
	v_div_scale_f32 v180, s[100:101], v97, v97, 1.0
	v_rcp_f32_e32 v181, v180
	v_div_scale_f32 v182, vcc, 1.0, v97, 1.0
	v_fma_f32 v183, -v180, v181, 1.0
	v_fmac_f32_e32 v181, v183, v181
	v_mul_f32_e32 v183, v182, v181
	v_fma_f32 v184, -v180, v183, v182
	v_fmac_f32_e32 v183, v184, v181
	v_fma_f32 v180, -v180, v183, v182
	v_div_fmas_f32 v180, v180, v181, v183
	v_div_fixup_f32 v97, v180, v97, 1.0
	v_div_scale_f32 v180, s[100:101], v98, v98, 1.0
	v_rcp_f32_e32 v181, v180
	v_div_scale_f32 v182, vcc, 1.0, v98, 1.0
	v_fma_f32 v183, -v180, v181, 1.0
	v_fmac_f32_e32 v181, v183, v181
	v_mul_f32_e32 v183, v182, v181
	v_fma_f32 v184, -v180, v183, v182
	v_fmac_f32_e32 v183, v184, v181
	v_fma_f32 v180, -v180, v183, v182
	v_div_fmas_f32 v180, v180, v181, v183
	v_div_fixup_f32 v98, v180, v98, 1.0
; __device__ __forceinline__ unsigned cvt_pk_bf16(float lo, float hi) { const f32x2c v = {lo, hi}; const bf16x2c b = __builtin_convertvector(v, bf16x2c); return __builtin_bit_cast(unsigned, b); }
; __device__ __forceinline__ float sigmoidf_(float x) { return 1.f / (1.f + __expf(-x)); }
;     __device__ __forceinline__ void operator()(const f32x4 (&acc)[2][2][4][2], const Unit& u, int wr, int wc, int fr, int fq) const {
;     ...
;                     const f32x4 v0 = acc[ai][bj][m][0] + b0, v1 = acc[ai][bj][m][1] + b1; float o[8];
; #pragma unroll
;                     for (int e = 0; e < 8; ++e) { float x = (e < 4) ? v0[e & 3] : v1[e & 3];
;                         if (kind == 0) x = -0.6065306597126334f * sigmoidf_(x);
;                         else if (kind == 1) x = sigmoidf_(x);
;                         o[e] = x; }
;                     u32x4 w; w.x = cvt_pk_bf16(o[0], o[1]); w.y = cvt_pk_bf16(o[2], o[3]); w.z = cvt_pk_bf16(o[4], o[5]); w.w = cvt_pk_bf16(o[6], o[7]);
;                     *(u32x4*)(O + row * 512 + col) = w; } }
	v_div_scale_f32 v180, s[100:101], v99, v99, 1.0
	v_rcp_f32_e32 v181, v180
	v_div_scale_f32 v182, vcc, 1.0, v99, 1.0
	v_fma_f32 v183, -v180, v181, 1.0
	v_fmac_f32_e32 v181, v183, v181
	v_mul_f32_e32 v183, v182, v181
	v_fma_f32 v184, -v180, v183, v182
	v_fmac_f32_e32 v183, v184, v181
	v_fma_f32 v180, -v180, v183, v182
	v_div_fmas_f32 v180, v180, v181, v183
	v_div_fixup_f32 v99, v180, v99, 1.0
	v_pk_mul_f32 v[100:101], v[100:101], v[198:199]
	v_pk_mul_f32 v[102:103], v[102:103], v[198:199]
	v_pk_mul_f32 v[96:97], v[96:97], v[198:199]
	v_pk_mul_f32 v[98:99], v[98:99], v[198:199]
	s_mov_b64 s[98:99], 0x20000
	v_lshl_add_u64 v[158:159], v[156:157], 0, s[98:99]
	v_cvt_pk_bf16_f32 v188, v100, v101
	v_cvt_pk_bf16_f32 v189, v102, v103
	v_cvt_pk_bf16_f32 v190, v96, v97
	v_cvt_pk_bf16_f32 v191, v98, v99
	global_store_dwordx4 v[158:159], v[188:191], off
	v_pk_add_f32 v[92:93], v[92:93], v[164:165]
	v_pk_add_f32 v[94:95], v[94:95], v[166:167]
	v_pk_add_f32 v[84:85], v[84:85], v[168:169]
	v_pk_add_f32 v[86:87], v[86:87], v[170:171]
	v_pk_mul_f32 v[92:93], v[92:93], v[196:197]
	v_pk_mul_f32 v[94:95], v[94:95], v[196:197]
	v_pk_mul_f32 v[84:85], v[84:85], v[196:197]
	v_pk_mul_f32 v[86:87], v[86:87], v[196:197]
	v_exp_f32_e32 v92, v92
	v_exp_f32_e32 v93, v93
	v_exp_f32_e32 v94, v94
	v_exp_f32_e32 v95, v95
	v_exp_f32_e32 v84, v84
	v_exp_f32_e32 v85, v85
	v_exp_f32_e32 v86, v86
	v_exp_f32_e32 v87, v87
	v_pk_add_f32 v[92:93], v[92:93], 1.0 op_sel_hi:[1,0]
	v_pk_add_f32 v[94:95], v[94:95], 1.0 op_sel_hi:[1,0]
	v_pk_add_f32 v[84:85], v[84:85], 1.0 op_sel_hi:[1,0]
	v_pk_add_f32 v[86:87], v[86:87], 1.0 op_sel_hi:[1,0]
	v_div_scale_f32 v180, s[100:101], v92, v92, 1.0
	v_rcp_f32_e32 v181, v180
	v_div_scale_f32 v182, vcc, 1.0, v92, 1.0
	v_fma_f32 v183, -v180, v181, 1.0
	v_fmac_f32_e32 v181, v183, v181
	v_mul_f32_e32 v183, v182, v181
	v_fma_f32 v184, -v180, v183, v182
	v_fmac_f32_e32 v183, v184, v181
	v_fma_f32 v180, -v180, v183, v182
	v_div_fmas_f32 v180, v180, v181, v183
	v_div_fixup_f32 v92, v180, v92, 1.0
	v_div_scale_f32 v180, s[100:101], v93, v93, 1.0
	v_rcp_f32_e32 v181, v180
	v_div_scale_f32 v182, vcc, 1.0, v93, 1.0
	v_fma_f32 v183, -v180, v181, 1.0
	v_fmac_f32_e32 v181, v183, v181
	v_mul_f32_e32 v183, v182, v181
	v_fma_f32 v184, -v180, v183, v182
	v_fmac_f32_e32 v183, v184, v181
	v_fma_f32 v180, -v180, v183, v182
	v_div_fmas_f32 v180, v180, v181, v183
	v_div_fixup_f32 v93, v180, v93, 1.0
	v_div_scale_f32 v180, s[100:101], v94, v94, 1.0
	v_rcp_f32_e32 v181, v180
	v_div_scale_f32 v182, vcc, 1.0, v94, 1.0
	v_fma_f32 v183, -v180, v181, 1.0
	v_fmac_f32_e32 v181, v183, v181
	v_mul_f32_e32 v183, v182, v181
	v_fma_f32 v184, -v180, v183, v182
	v_fmac_f32_e32 v183, v184, v181
	v_fma_f32 v180, -v180, v183, v182
	v_div_fmas_f32 v180, v180, v181, v183
	v_div_fixup_f32 v94, v180, v94, 1.0
	v_div_scale_f32 v180, s[100:101], v95, v95, 1.0
	v_rcp_f32_e32 v181, v180
	v_div_scale_f32 v182, vcc, 1.0, v95, 1.0
	v_fma_f32 v183, -v180, v181, 1.0
	v_fmac_f32_e32 v181, v183, v181
	v_mul_f32_e32 v183, v182, v181
	v_fma_f32 v184, -v180, v183, v182
	v_fmac_f32_e32 v183, v184, v181
	v_fma_f32 v180, -v180, v183, v182
	v_div_fmas_f32 v180, v180, v181, v183
	v_div_fixup_f32 v95, v180, v95, 1.0
	v_div_scale_f32 v180, s[100:101], v84, v84, 1.0
	v_rcp_f32_e32 v181, v180
	v_div_scale_f32 v182, vcc, 1.0, v84, 1.0
	v_fma_f32 v183, -v180, v181, 1.0
	v_fmac_f32_e32 v181, v183, v181
	v_mul_f32_e32 v183, v182, v181
	v_fma_f32 v184, -v180, v183, v182
	v_fmac_f32_e32 v183, v184, v181
	v_fma_f32 v180, -v180, v183, v182
	v_div_fmas_f32 v180, v180, v181, v183
	v_div_fixup_f32 v84, v180, v84, 1.0
	v_div_scale_f32 v180, s[100:101], v85, v85, 1.0
	v_rcp_f32_e32 v181, v180
	v_div_scale_f32 v182, vcc, 1.0, v85, 1.0
	v_fma_f32 v183, -v180, v181, 1.0
	v_fmac_f32_e32 v181, v183, v181
	v_mul_f32_e32 v183, v182, v181
	v_fma_f32 v184, -v180, v183, v182
	v_fmac_f32_e32 v183, v184, v181
	v_fma_f32 v180, -v180, v183, v182
	v_div_fmas_f32 v180, v180, v181, v183
	v_div_fixup_f32 v85, v180, v85, 1.0
	v_div_scale_f32 v180, s[100:101], v86, v86, 1.0
	v_rcp_f32_e32 v181, v180
	v_div_scale_f32 v182, vcc, 1.0, v86, 1.0
	v_fma_f32 v183, -v180, v181, 1.0
	v_fmac_f32_e32 v181, v183, v181
	v_mul_f32_e32 v183, v182, v181
	v_fma_f32 v184, -v180, v183, v182
	v_fmac_f32_e32 v183, v184, v181
	v_fma_f32 v180, -v180, v183, v182
	v_div_fmas_f32 v180, v180, v181, v183
	v_div_fixup_f32 v86, v180, v86, 1.0
	v_div_scale_f32 v180, s[100:101], v87, v87, 1.0
	v_rcp_f32_e32 v181, v180
	v_div_scale_f32 v182, vcc, 1.0, v87, 1.0
	v_fma_f32 v183, -v180, v181, 1.0
	v_fmac_f32_e32 v181, v183, v181
	v_mul_f32_e32 v183, v182, v181
	v_fma_f32 v184, -v180, v183, v182
	v_fmac_f32_e32 v183, v184, v181
	v_fma_f32 v180, -v180, v183, v182
	v_div_fmas_f32 v180, v180, v181, v183
	v_div_fixup_f32 v87, v180, v87, 1.0
	v_pk_mul_f32 v[92:93], v[92:93], v[198:199]
	v_pk_mul_f32 v[94:95], v[94:95], v[198:199]
	v_pk_mul_f32 v[84:85], v[84:85], v[198:199]
	v_pk_mul_f32 v[86:87], v[86:87], v[198:199]
	s_mov_b64 s[98:99], 0x24000
	v_lshl_add_u64 v[158:159], v[156:157], 0, s[98:99]
	v_cvt_pk_bf16_f32 v192, v92, v93
	v_cvt_pk_bf16_f32 v193, v94, v95
	v_cvt_pk_bf16_f32 v194, v84, v85
	v_cvt_pk_bf16_f32 v195, v86, v87
	global_store_dwordx4 v[158:159], v[192:195], off
	v_pk_add_f32 v[76:77], v[76:77], v[164:165]
	v_pk_add_f32 v[78:79], v[78:79], v[166:167]
	v_pk_add_f32 v[72:73], v[72:73], v[168:169]
	v_pk_add_f32 v[74:75], v[74:75], v[170:171]
	v_pk_mul_f32 v[76:77], v[76:77], v[196:197]
	v_pk_mul_f32 v[78:79], v[78:79], v[196:197]
	v_pk_mul_f32 v[72:73], v[72:73], v[196:197]
	v_pk_mul_f32 v[74:75], v[74:75], v[196:197]
	v_exp_f32_e32 v76, v76
	v_exp_f32_e32 v77, v77
; __device__ __forceinline__ unsigned cvt_pk_bf16(float lo, float hi) { const f32x2c v = {lo, hi}; const bf16x2c b = __builtin_convertvector(v, bf16x2c); return __builtin_bit_cast(unsigned, b); }
; __device__ __forceinline__ float sigmoidf_(float x) { return 1.f / (1.f + __expf(-x)); }
;     __device__ __forceinline__ void operator()(const f32x4 (&acc)[2][2][4][2], const Unit& u, int wr, int wc, int fr, int fq) const {
;     ...
;                     const f32x4 v0 = acc[ai][bj][m][0] + b0, v1 = acc[ai][bj][m][1] + b1; float o[8];
; #pragma unroll
;                     for (int e = 0; e < 8; ++e) { float x = (e < 4) ? v0[e & 3] : v1[e & 3];
;                         if (kind == 0) x = -0.6065306597126334f * sigmoidf_(x);
;                         else if (kind == 1) x = sigmoidf_(x);
;                         o[e] = x; }
;                     u32x4 w; w.x = cvt_pk_bf16(o[0], o[1]); w.y = cvt_pk_bf16(o[2], o[3]); w.z = cvt_pk_bf16(o[4], o[5]); w.w = cvt_pk_bf16(o[6], o[7]);
;                     *(u32x4*)(O + row * 512 + col) = w; } }
	v_exp_f32_e32 v78, v78
	v_exp_f32_e32 v79, v79
	v_exp_f32_e32 v72, v72
	v_exp_f32_e32 v73, v73
	v_exp_f32_e32 v74, v74
	v_exp_f32_e32 v75, v75
	v_pk_add_f32 v[76:77], v[76:77], 1.0 op_sel_hi:[1,0]
	v_pk_add_f32 v[78:79], v[78:79], 1.0 op_sel_hi:[1,0]
	v_pk_add_f32 v[72:73], v[72:73], 1.0 op_sel_hi:[1,0]
	v_pk_add_f32 v[74:75], v[74:75], 1.0 op_sel_hi:[1,0]
	v_div_scale_f32 v180, s[100:101], v76, v76, 1.0
	v_rcp_f32_e32 v181, v180
	v_div_scale_f32 v182, vcc, 1.0, v76, 1.0
	v_fma_f32 v183, -v180, v181, 1.0
	v_fmac_f32_e32 v181, v183, v181
	v_mul_f32_e32 v183, v182, v181
	v_fma_f32 v184, -v180, v183, v182
	v_fmac_f32_e32 v183, v184, v181
	v_fma_f32 v180, -v180, v183, v182
	v_div_fmas_f32 v180, v180, v181, v183
	v_div_fixup_f32 v76, v180, v76, 1.0
	v_div_scale_f32 v180, s[100:101], v77, v77, 1.0
	v_rcp_f32_e32 v181, v180
	v_div_scale_f32 v182, vcc, 1.0, v77, 1.0
	v_fma_f32 v183, -v180, v181, 1.0
	v_fmac_f32_e32 v181, v183, v181
	v_mul_f32_e32 v183, v182, v181
	v_fma_f32 v184, -v180, v183, v182
	v_fmac_f32_e32 v183, v184, v181
	v_fma_f32 v180, -v180, v183, v182
	v_div_fmas_f32 v180, v180, v181, v183
	v_div_fixup_f32 v77, v180, v77, 1.0
	v_div_scale_f32 v180, s[100:101], v78, v78, 1.0
	v_rcp_f32_e32 v181, v180
	v_div_scale_f32 v182, vcc, 1.0, v78, 1.0
	v_fma_f32 v183, -v180, v181, 1.0
	v_fmac_f32_e32 v181, v183, v181
	v_mul_f32_e32 v183, v182, v181
	v_fma_f32 v184, -v180, v183, v182
	v_fmac_f32_e32 v183, v184, v181
	v_fma_f32 v180, -v180, v183, v182
	v_div_fmas_f32 v180, v180, v181, v183
	v_div_fixup_f32 v78, v180, v78, 1.0
	v_div_scale_f32 v180, s[100:101], v79, v79, 1.0
	v_rcp_f32_e32 v181, v180
	v_div_scale_f32 v182, vcc, 1.0, v79, 1.0
	v_fma_f32 v183, -v180, v181, 1.0
	v_fmac_f32_e32 v181, v183, v181
	v_mul_f32_e32 v183, v182, v181
	v_fma_f32 v184, -v180, v183, v182
	v_fmac_f32_e32 v183, v184, v181
	v_fma_f32 v180, -v180, v183, v182
	v_div_fmas_f32 v180, v180, v181, v183
	v_div_fixup_f32 v79, v180, v79, 1.0
	v_div_scale_f32 v180, s[100:101], v72, v72, 1.0
	v_rcp_f32_e32 v181, v180
	v_div_scale_f32 v182, vcc, 1.0, v72, 1.0
	v_fma_f32 v183, -v180, v181, 1.0
	v_fmac_f32_e32 v181, v183, v181
	v_mul_f32_e32 v183, v182, v181
	v_fma_f32 v184, -v180, v183, v182
	v_fmac_f32_e32 v183, v184, v181
	v_fma_f32 v180, -v180, v183, v182
	v_div_fmas_f32 v180, v180, v181, v183
	v_div_fixup_f32 v72, v180, v72, 1.0
	v_div_scale_f32 v180, s[100:101], v73, v73, 1.0
	v_rcp_f32_e32 v181, v180
	v_div_scale_f32 v182, vcc, 1.0, v73, 1.0
	v_fma_f32 v183, -v180, v181, 1.0
	v_fmac_f32_e32 v181, v183, v181
	v_mul_f32_e32 v183, v182, v181
	v_fma_f32 v184, -v180, v183, v182
	v_fmac_f32_e32 v183, v184, v181
	v_fma_f32 v180, -v180, v183, v182
	v_div_fmas_f32 v180, v180, v181, v183
	v_div_fixup_f32 v73, v180, v73, 1.0
	v_div_scale_f32 v180, s[100:101], v74, v74, 1.0
	v_rcp_f32_e32 v181, v180
	v_div_scale_f32 v182, vcc, 1.0, v74, 1.0
	v_fma_f32 v183, -v180, v181, 1.0
	v_fmac_f32_e32 v181, v183, v181
	v_mul_f32_e32 v183, v182, v181
	v_fma_f32 v184, -v180, v183, v182
	v_fmac_f32_e32 v183, v184, v181
	v_fma_f32 v180, -v180, v183, v182
	v_div_fmas_f32 v180, v180, v181, v183
	v_div_fixup_f32 v74, v180, v74, 1.0
	v_div_scale_f32 v180, s[100:101], v75, v75, 1.0
	v_rcp_f32_e32 v181, v180
	v_div_scale_f32 v182, vcc, 1.0, v75, 1.0
	v_fma_f32 v183, -v180, v181, 1.0
	v_fmac_f32_e32 v181, v183, v181
	v_mul_f32_e32 v183, v182, v181
	v_fma_f32 v184, -v180, v183, v182
	v_fmac_f32_e32 v183, v184, v181
	v_fma_f32 v180, -v180, v183, v182
	v_div_fmas_f32 v180, v180, v181, v183
	v_div_fixup_f32 v75, v180, v75, 1.0
	v_pk_mul_f32 v[76:77], v[76:77], v[198:199]
	v_pk_mul_f32 v[78:79], v[78:79], v[198:199]
	v_pk_mul_f32 v[72:73], v[72:73], v[198:199]
	v_pk_mul_f32 v[74:75], v[74:75], v[198:199]
	s_mov_b64 s[98:99], 0x28000
	v_lshl_add_u64 v[158:159], v[156:157], 0, s[98:99]
	v_cvt_pk_bf16_f32 v188, v76, v77
	v_cvt_pk_bf16_f32 v189, v78, v79
	v_cvt_pk_bf16_f32 v190, v72, v73
	v_cvt_pk_bf16_f32 v191, v74, v75
	global_store_dwordx4 v[158:159], v[188:191], off
	v_pk_add_f32 v[68:69], v[68:69], v[164:165]
	v_pk_add_f32 v[70:71], v[70:71], v[166:167]
	v_pk_add_f32 v[64:65], v[64:65], v[168:169]
	v_pk_add_f32 v[66:67], v[66:67], v[170:171]
	v_pk_mul_f32 v[68:69], v[68:69], v[196:197]
	v_pk_mul_f32 v[70:71], v[70:71], v[196:197]
	v_pk_mul_f32 v[64:65], v[64:65], v[196:197]
	v_pk_mul_f32 v[66:67], v[66:67], v[196:197]
	v_exp_f32_e32 v68, v68
	v_exp_f32_e32 v69, v69
	v_exp_f32_e32 v70, v70
	v_exp_f32_e32 v71, v71
	v_exp_f32_e32 v64, v64
	v_exp_f32_e32 v65, v65
	v_exp_f32_e32 v66, v66
	v_exp_f32_e32 v67, v67
	v_pk_add_f32 v[68:69], v[68:69], 1.0 op_sel_hi:[1,0]
	v_pk_add_f32 v[70:71], v[70:71], 1.0 op_sel_hi:[1,0]
	v_pk_add_f32 v[64:65], v[64:65], 1.0 op_sel_hi:[1,0]
	v_pk_add_f32 v[66:67], v[66:67], 1.0 op_sel_hi:[1,0]
	v_div_scale_f32 v180, s[100:101], v68, v68, 1.0
	v_rcp_f32_e32 v181, v180
	v_div_scale_f32 v182, vcc, 1.0, v68, 1.0
	v_fma_f32 v183, -v180, v181, 1.0
	v_fmac_f32_e32 v181, v183, v181
	v_mul_f32_e32 v183, v182, v181
	v_fma_f32 v184, -v180, v183, v182
	v_fmac_f32_e32 v183, v184, v181
	v_fma_f32 v180, -v180, v183, v182
	v_div_fmas_f32 v180, v180, v181, v183
	v_div_fixup_f32 v68, v180, v68, 1.0
	v_div_scale_f32 v180, s[100:101], v69, v69, 1.0
	v_rcp_f32_e32 v181, v180
	v_div_scale_f32 v182, vcc, 1.0, v69, 1.0
	v_fma_f32 v183, -v180, v181, 1.0
	v_fmac_f32_e32 v181, v183, v181
	v_mul_f32_e32 v183, v182, v181
	v_fma_f32 v184, -v180, v183, v182
	v_fmac_f32_e32 v183, v184, v181
	v_fma_f32 v180, -v180, v183, v182
	v_div_fmas_f32 v180, v180, v181, v183
	v_div_fixup_f32 v69, v180, v69, 1.0
	v_div_scale_f32 v180, s[100:101], v70, v70, 1.0
	v_rcp_f32_e32 v181, v180
	v_div_scale_f32 v182, vcc, 1.0, v70, 1.0
; __device__ __forceinline__ unsigned cvt_pk_bf16(float lo, float hi) { const f32x2c v = {lo, hi}; const bf16x2c b = __builtin_convertvector(v, bf16x2c); return __builtin_bit_cast(unsigned, b); }
; __device__ __forceinline__ float sigmoidf_(float x) { return 1.f / (1.f + __expf(-x)); }
;     __device__ __forceinline__ void operator()(const f32x4 (&acc)[2][2][4][2], const Unit& u, int wr, int wc, int fr, int fq) const {
;     ...
;                     const f32x4 v0 = acc[ai][bj][m][0] + b0, v1 = acc[ai][bj][m][1] + b1; float o[8];
; #pragma unroll
;                     for (int e = 0; e < 8; ++e) { float x = (e < 4) ? v0[e & 3] : v1[e & 3];
;                         if (kind == 0) x = -0.6065306597126334f * sigmoidf_(x);
;                         else if (kind == 1) x = sigmoidf_(x);
;                         o[e] = x; }
;                     u32x4 w; w.x = cvt_pk_bf16(o[0], o[1]); w.y = cvt_pk_bf16(o[2], o[3]); w.z = cvt_pk_bf16(o[4], o[5]); w.w = cvt_pk_bf16(o[6], o[7]);
;                     *(u32x4*)(O + row * 512 + col) = w; } }
	v_fma_f32 v183, -v180, v181, 1.0
	v_fmac_f32_e32 v181, v183, v181
	v_mul_f32_e32 v183, v182, v181
	v_fma_f32 v184, -v180, v183, v182
	v_fmac_f32_e32 v183, v184, v181
	v_fma_f32 v180, -v180, v183, v182
	v_div_fmas_f32 v180, v180, v181, v183
	v_div_fixup_f32 v70, v180, v70, 1.0
	v_div_scale_f32 v180, s[100:101], v71, v71, 1.0
	v_rcp_f32_e32 v181, v180
	v_div_scale_f32 v182, vcc, 1.0, v71, 1.0
	v_fma_f32 v183, -v180, v181, 1.0
	v_fmac_f32_e32 v181, v183, v181
	v_mul_f32_e32 v183, v182, v181
	v_fma_f32 v184, -v180, v183, v182
	v_fmac_f32_e32 v183, v184, v181
	v_fma_f32 v180, -v180, v183, v182
	v_div_fmas_f32 v180, v180, v181, v183
	v_div_fixup_f32 v71, v180, v71, 1.0
	v_div_scale_f32 v180, s[100:101], v64, v64, 1.0
	v_rcp_f32_e32 v181, v180
	v_div_scale_f32 v182, vcc, 1.0, v64, 1.0
	v_fma_f32 v183, -v180, v181, 1.0
	v_fmac_f32_e32 v181, v183, v181
	v_mul_f32_e32 v183, v182, v181
	v_fma_f32 v184, -v180, v183, v182
	v_fmac_f32_e32 v183, v184, v181
	v_fma_f32 v180, -v180, v183, v182
	v_div_fmas_f32 v180, v180, v181, v183
	v_div_fixup_f32 v64, v180, v64, 1.0
	v_div_scale_f32 v180, s[100:101], v65, v65, 1.0
	v_rcp_f32_e32 v181, v180
	v_div_scale_f32 v182, vcc, 1.0, v65, 1.0
	v_fma_f32 v183, -v180, v181, 1.0
	v_fmac_f32_e32 v181, v183, v181
	v_mul_f32_e32 v183, v182, v181
	v_fma_f32 v184, -v180, v183, v182
	v_fmac_f32_e32 v183, v184, v181
	v_fma_f32 v180, -v180, v183, v182
	v_div_fmas_f32 v180, v180, v181, v183
	v_div_fixup_f32 v65, v180, v65, 1.0
	v_div_scale_f32 v180, s[100:101], v66, v66, 1.0
	v_rcp_f32_e32 v181, v180
	v_div_scale_f32 v182, vcc, 1.0, v66, 1.0
	v_fma_f32 v183, -v180, v181, 1.0
	v_fmac_f32_e32 v181, v183, v181
	v_mul_f32_e32 v183, v182, v181
	v_fma_f32 v184, -v180, v183, v182
	v_fmac_f32_e32 v183, v184, v181
	v_fma_f32 v180, -v180, v183, v182
	v_div_fmas_f32 v180, v180, v181, v183
	v_div_fixup_f32 v66, v180, v66, 1.0
	v_div_scale_f32 v180, s[100:101], v67, v67, 1.0
	v_rcp_f32_e32 v181, v180
	v_div_scale_f32 v182, vcc, 1.0, v67, 1.0
	v_fma_f32 v183, -v180, v181, 1.0
	v_fmac_f32_e32 v181, v183, v181
	v_mul_f32_e32 v183, v182, v181
	v_fma_f32 v184, -v180, v183, v182
	v_fmac_f32_e32 v183, v184, v181
	v_fma_f32 v180, -v180, v183, v182
	v_div_fmas_f32 v180, v180, v181, v183
	v_div_fixup_f32 v67, v180, v67, 1.0
	v_pk_mul_f32 v[68:69], v[68:69], v[198:199]
	v_pk_mul_f32 v[70:71], v[70:71], v[198:199]
	v_pk_mul_f32 v[64:65], v[64:65], v[198:199]
	v_pk_mul_f32 v[66:67], v[66:67], v[198:199]
	s_mov_b64 s[98:99], 0x2c000
	v_lshl_add_u64 v[158:159], v[156:157], 0, s[98:99]
	v_cvt_pk_bf16_f32 v192, v68, v69
	v_cvt_pk_bf16_f32 v193, v70, v71
	v_cvt_pk_bf16_f32 v194, v64, v65
	v_cvt_pk_bf16_f32 v195, v66, v67
	global_store_dwordx4 v[158:159], v[192:195], off
	v_pk_add_f32 v[60:61], v[60:61], v[172:173]
	v_pk_add_f32 v[62:63], v[62:63], v[174:175]
	v_pk_add_f32 v[56:57], v[56:57], v[176:177]
	v_pk_add_f32 v[58:59], v[58:59], v[178:179]
	v_pk_mul_f32 v[60:61], v[60:61], v[196:197]
	v_pk_mul_f32 v[62:63], v[62:63], v[196:197]
	v_pk_mul_f32 v[56:57], v[56:57], v[196:197]
	v_pk_mul_f32 v[58:59], v[58:59], v[196:197]
	v_exp_f32_e32 v60, v60
	v_exp_f32_e32 v61, v61
	v_exp_f32_e32 v62, v62
	v_exp_f32_e32 v63, v63
	v_exp_f32_e32 v56, v56
	v_exp_f32_e32 v57, v57
	v_exp_f32_e32 v58, v58
	v_exp_f32_e32 v59, v59
	v_pk_add_f32 v[60:61], v[60:61], 1.0 op_sel_hi:[1,0]
	v_pk_add_f32 v[62:63], v[62:63], 1.0 op_sel_hi:[1,0]
	v_pk_add_f32 v[56:57], v[56:57], 1.0 op_sel_hi:[1,0]
	v_pk_add_f32 v[58:59], v[58:59], 1.0 op_sel_hi:[1,0]
	v_div_scale_f32 v180, s[100:101], v60, v60, 1.0
	v_rcp_f32_e32 v181, v180
	v_div_scale_f32 v182, vcc, 1.0, v60, 1.0
	v_fma_f32 v183, -v180, v181, 1.0
	v_fmac_f32_e32 v181, v183, v181
	v_mul_f32_e32 v183, v182, v181
	v_fma_f32 v184, -v180, v183, v182
	v_fmac_f32_e32 v183, v184, v181
	v_fma_f32 v180, -v180, v183, v182
	v_div_fmas_f32 v180, v180, v181, v183
	v_div_fixup_f32 v60, v180, v60, 1.0
	v_div_scale_f32 v180, s[100:101], v61, v61, 1.0
	v_rcp_f32_e32 v181, v180
	v_div_scale_f32 v182, vcc, 1.0, v61, 1.0
	v_fma_f32 v183, -v180, v181, 1.0
	v_fmac_f32_e32 v181, v183, v181
	v_mul_f32_e32 v183, v182, v181
	v_fma_f32 v184, -v180, v183, v182
	v_fmac_f32_e32 v183, v184, v181
	v_fma_f32 v180, -v180, v183, v182
	v_div_fmas_f32 v180, v180, v181, v183
	v_div_fixup_f32 v61, v180, v61, 1.0
	v_div_scale_f32 v180, s[100:101], v62, v62, 1.0
	v_rcp_f32_e32 v181, v180
	v_div_scale_f32 v182, vcc, 1.0, v62, 1.0
	v_fma_f32 v183, -v180, v181, 1.0
	v_fmac_f32_e32 v181, v183, v181
	v_mul_f32_e32 v183, v182, v181
	v_fma_f32 v184, -v180, v183, v182
	v_fmac_f32_e32 v183, v184, v181
	v_fma_f32 v180, -v180, v183, v182
	v_div_fmas_f32 v180, v180, v181, v183
	v_div_fixup_f32 v62, v180, v62, 1.0
	v_div_scale_f32 v180, s[100:101], v63, v63, 1.0
	v_rcp_f32_e32 v181, v180
	v_div_scale_f32 v182, vcc, 1.0, v63, 1.0
	v_fma_f32 v183, -v180, v181, 1.0
	v_fmac_f32_e32 v181, v183, v181
	v_mul_f32_e32 v183, v182, v181
	v_fma_f32 v184, -v180, v183, v182
	v_fmac_f32_e32 v183, v184, v181
	v_fma_f32 v180, -v180, v183, v182
	v_div_fmas_f32 v180, v180, v181, v183
	v_div_fixup_f32 v63, v180, v63, 1.0
	v_div_scale_f32 v180, s[100:101], v56, v56, 1.0
	v_rcp_f32_e32 v181, v180
	v_div_scale_f32 v182, vcc, 1.0, v56, 1.0
	v_fma_f32 v183, -v180, v181, 1.0
	v_fmac_f32_e32 v181, v183, v181
	v_mul_f32_e32 v183, v182, v181
	v_fma_f32 v184, -v180, v183, v182
	v_fmac_f32_e32 v183, v184, v181
	v_fma_f32 v180, -v180, v183, v182
	v_div_fmas_f32 v180, v180, v181, v183
	v_div_fixup_f32 v56, v180, v56, 1.0
	v_div_scale_f32 v180, s[100:101], v57, v57, 1.0
	v_rcp_f32_e32 v181, v180
	v_div_scale_f32 v182, vcc, 1.0, v57, 1.0
	v_fma_f32 v183, -v180, v181, 1.0
	v_fmac_f32_e32 v181, v183, v181
; __device__ __forceinline__ unsigned cvt_pk_bf16(float lo, float hi) { const f32x2c v = {lo, hi}; const bf16x2c b = __builtin_convertvector(v, bf16x2c); return __builtin_bit_cast(unsigned, b); }
; __device__ __forceinline__ float sigmoidf_(float x) { return 1.f / (1.f + __expf(-x)); }
;     __device__ __forceinline__ void operator()(const f32x4 (&acc)[2][2][4][2], const Unit& u, int wr, int wc, int fr, int fq) const {
;     ...
;                     const f32x4 v0 = acc[ai][bj][m][0] + b0, v1 = acc[ai][bj][m][1] + b1; float o[8];
; #pragma unroll
;                     for (int e = 0; e < 8; ++e) { float x = (e < 4) ? v0[e & 3] : v1[e & 3];
;                         if (kind == 0) x = -0.6065306597126334f * sigmoidf_(x);
;                         else if (kind == 1) x = sigmoidf_(x);
;                         o[e] = x; }
;                     u32x4 w; w.x = cvt_pk_bf16(o[0], o[1]); w.y = cvt_pk_bf16(o[2], o[3]); w.z = cvt_pk_bf16(o[4], o[5]); w.w = cvt_pk_bf16(o[6], o[7]);
;                     *(u32x4*)(O + row * 512 + col) = w; } }
	v_mul_f32_e32 v183, v182, v181
	v_fma_f32 v184, -v180, v183, v182
	v_fmac_f32_e32 v183, v184, v181
	v_fma_f32 v180, -v180, v183, v182
	v_div_fmas_f32 v180, v180, v181, v183
	v_div_fixup_f32 v57, v180, v57, 1.0
	v_div_scale_f32 v180, s[100:101], v58, v58, 1.0
	v_rcp_f32_e32 v181, v180
	v_div_scale_f32 v182, vcc, 1.0, v58, 1.0
	v_fma_f32 v183, -v180, v181, 1.0
	v_fmac_f32_e32 v181, v183, v181
	v_mul_f32_e32 v183, v182, v181
	v_fma_f32 v184, -v180, v183, v182
	v_fmac_f32_e32 v183, v184, v181
	v_fma_f32 v180, -v180, v183, v182
	v_div_fmas_f32 v180, v180, v181, v183
	v_div_fixup_f32 v58, v180, v58, 1.0
	v_div_scale_f32 v180, s[100:101], v59, v59, 1.0
	v_rcp_f32_e32 v181, v180
	v_div_scale_f32 v182, vcc, 1.0, v59, 1.0
	v_fma_f32 v183, -v180, v181, 1.0
	v_fmac_f32_e32 v181, v183, v181
	v_mul_f32_e32 v183, v182, v181
	v_fma_f32 v184, -v180, v183, v182
	v_fmac_f32_e32 v183, v184, v181
	v_fma_f32 v180, -v180, v183, v182
	v_div_fmas_f32 v180, v180, v181, v183
	v_div_fixup_f32 v59, v180, v59, 1.0
	v_pk_mul_f32 v[60:61], v[60:61], v[198:199]
	v_pk_mul_f32 v[62:63], v[62:63], v[198:199]
	v_pk_mul_f32 v[56:57], v[56:57], v[198:199]
	v_pk_mul_f32 v[58:59], v[58:59], v[198:199]
	v_cvt_pk_bf16_f32 v188, v60, v61
	v_cvt_pk_bf16_f32 v189, v62, v63
	v_cvt_pk_bf16_f32 v190, v56, v57
	v_cvt_pk_bf16_f32 v191, v58, v59
	global_store_dwordx4 v[156:157], v[188:191], off offset:256
	v_pk_add_f32 v[52:53], v[52:53], v[172:173]
	v_pk_add_f32 v[54:55], v[54:55], v[174:175]
	v_pk_add_f32 v[48:49], v[48:49], v[176:177]
	v_pk_add_f32 v[50:51], v[50:51], v[178:179]
	v_pk_mul_f32 v[52:53], v[52:53], v[196:197]
	v_pk_mul_f32 v[54:55], v[54:55], v[196:197]
	v_pk_mul_f32 v[48:49], v[48:49], v[196:197]
	v_pk_mul_f32 v[50:51], v[50:51], v[196:197]
	v_exp_f32_e32 v52, v52
	v_exp_f32_e32 v53, v53
	v_exp_f32_e32 v54, v54
	v_exp_f32_e32 v55, v55
	v_exp_f32_e32 v48, v48
	v_exp_f32_e32 v49, v49
	v_exp_f32_e32 v50, v50
	v_exp_f32_e32 v51, v51
	v_pk_add_f32 v[52:53], v[52:53], 1.0 op_sel_hi:[1,0]
	v_pk_add_f32 v[54:55], v[54:55], 1.0 op_sel_hi:[1,0]
	v_pk_add_f32 v[48:49], v[48:49], 1.0 op_sel_hi:[1,0]
	v_pk_add_f32 v[50:51], v[50:51], 1.0 op_sel_hi:[1,0]
	v_div_scale_f32 v180, s[100:101], v52, v52, 1.0
	v_rcp_f32_e32 v181, v180
	v_div_scale_f32 v182, vcc, 1.0, v52, 1.0
	v_fma_f32 v183, -v180, v181, 1.0
	v_fmac_f32_e32 v181, v183, v181
	v_mul_f32_e32 v183, v182, v181
	v_fma_f32 v184, -v180, v183, v182
	v_fmac_f32_e32 v183, v184, v181
	v_fma_f32 v180, -v180, v183, v182
	v_div_fmas_f32 v180, v180, v181, v183
	v_div_fixup_f32 v52, v180, v52, 1.0
	v_div_scale_f32 v180, s[100:101], v53, v53, 1.0
	v_rcp_f32_e32 v181, v180
	v_div_scale_f32 v182, vcc, 1.0, v53, 1.0
	v_fma_f32 v183, -v180, v181, 1.0
	v_fmac_f32_e32 v181, v183, v181
	v_mul_f32_e32 v183, v182, v181
	v_fma_f32 v184, -v180, v183, v182
	v_fmac_f32_e32 v183, v184, v181
	v_fma_f32 v180, -v180, v183, v182
	v_div_fmas_f32 v180, v180, v181, v183
	v_div_fixup_f32 v53, v180, v53, 1.0
	v_div_scale_f32 v180, s[100:101], v54, v54, 1.0
	v_rcp_f32_e32 v181, v180
	v_div_scale_f32 v182, vcc, 1.0, v54, 1.0
	v_fma_f32 v183, -v180, v181, 1.0
	v_fmac_f32_e32 v181, v183, v181
	v_mul_f32_e32 v183, v182, v181
	v_fma_f32 v184, -v180, v183, v182
	v_fmac_f32_e32 v183, v184, v181
	v_fma_f32 v180, -v180, v183, v182
	v_div_fmas_f32 v180, v180, v181, v183
	v_div_fixup_f32 v54, v180, v54, 1.0
	v_div_scale_f32 v180, s[100:101], v55, v55, 1.0
	v_rcp_f32_e32 v181, v180
	v_div_scale_f32 v182, vcc, 1.0, v55, 1.0
	v_fma_f32 v183, -v180, v181, 1.0
	v_fmac_f32_e32 v181, v183, v181
	v_mul_f32_e32 v183, v182, v181
	v_fma_f32 v184, -v180, v183, v182
	v_fmac_f32_e32 v183, v184, v181
	v_fma_f32 v180, -v180, v183, v182
	v_div_fmas_f32 v180, v180, v181, v183
	v_div_fixup_f32 v55, v180, v55, 1.0
	v_div_scale_f32 v180, s[100:101], v48, v48, 1.0
	v_rcp_f32_e32 v181, v180
	v_div_scale_f32 v182, vcc, 1.0, v48, 1.0
	v_fma_f32 v183, -v180, v181, 1.0
	v_fmac_f32_e32 v181, v183, v181
	v_mul_f32_e32 v183, v182, v181
	v_fma_f32 v184, -v180, v183, v182
	v_fmac_f32_e32 v183, v184, v181
	v_fma_f32 v180, -v180, v183, v182
	v_div_fmas_f32 v180, v180, v181, v183
	v_div_fixup_f32 v48, v180, v48, 1.0
	v_div_scale_f32 v180, s[100:101], v49, v49, 1.0
	v_rcp_f32_e32 v181, v180
	v_div_scale_f32 v182, vcc, 1.0, v49, 1.0
	v_fma_f32 v183, -v180, v181, 1.0
	v_fmac_f32_e32 v181, v183, v181
	v_mul_f32_e32 v183, v182, v181
	v_fma_f32 v184, -v180, v183, v182
	v_fmac_f32_e32 v183, v184, v181
	v_fma_f32 v180, -v180, v183, v182
	v_div_fmas_f32 v180, v180, v181, v183
	v_div_fixup_f32 v49, v180, v49, 1.0
	v_div_scale_f32 v180, s[100:101], v50, v50, 1.0
	v_rcp_f32_e32 v181, v180
	v_div_scale_f32 v182, vcc, 1.0, v50, 1.0
	v_fma_f32 v183, -v180, v181, 1.0
	v_fmac_f32_e32 v181, v183, v181
	v_mul_f32_e32 v183, v182, v181
	v_fma_f32 v184, -v180, v183, v182
	v_fmac_f32_e32 v183, v184, v181
	v_fma_f32 v180, -v180, v183, v182
	v_div_fmas_f32 v180, v180, v181, v183
	v_div_fixup_f32 v50, v180, v50, 1.0
	v_div_scale_f32 v180, s[100:101], v51, v51, 1.0
	v_rcp_f32_e32 v181, v180
	v_div_scale_f32 v182, vcc, 1.0, v51, 1.0
	v_fma_f32 v183, -v180, v181, 1.0
	v_fmac_f32_e32 v181, v183, v181
	v_mul_f32_e32 v183, v182, v181
	v_fma_f32 v184, -v180, v183, v182
	v_fmac_f32_e32 v183, v184, v181
	v_fma_f32 v180, -v180, v183, v182
	v_div_fmas_f32 v180, v180, v181, v183
	v_div_fixup_f32 v51, v180, v51, 1.0
	v_pk_mul_f32 v[52:53], v[52:53], v[198:199]
	v_pk_mul_f32 v[54:55], v[54:55], v[198:199]
	v_pk_mul_f32 v[48:49], v[48:49], v[198:199]
	v_pk_mul_f32 v[50:51], v[50:51], v[198:199]
	s_mov_b64 s[98:99], 0x4000
	v_lshl_add_u64 v[158:159], v[156:157], 0, s[98:99]
	v_cvt_pk_bf16_f32 v192, v52, v53
	v_cvt_pk_bf16_f32 v193, v54, v55
; __device__ __forceinline__ unsigned cvt_pk_bf16(float lo, float hi) { const f32x2c v = {lo, hi}; const bf16x2c b = __builtin_convertvector(v, bf16x2c); return __builtin_bit_cast(unsigned, b); }
; __device__ __forceinline__ float sigmoidf_(float x) { return 1.f / (1.f + __expf(-x)); }
;     __device__ __forceinline__ void operator()(const f32x4 (&acc)[2][2][4][2], const Unit& u, int wr, int wc, int fr, int fq) const {
;     ...
;                     const f32x4 v0 = acc[ai][bj][m][0] + b0, v1 = acc[ai][bj][m][1] + b1; float o[8];
; #pragma unroll
;                     for (int e = 0; e < 8; ++e) { float x = (e < 4) ? v0[e & 3] : v1[e & 3];
;                         if (kind == 0) x = -0.6065306597126334f * sigmoidf_(x);
;                         else if (kind == 1) x = sigmoidf_(x);
;                         o[e] = x; }
;                     u32x4 w; w.x = cvt_pk_bf16(o[0], o[1]); w.y = cvt_pk_bf16(o[2], o[3]); w.z = cvt_pk_bf16(o[4], o[5]); w.w = cvt_pk_bf16(o[6], o[7]);
;                     *(u32x4*)(O + row * 512 + col) = w; } }
	v_cvt_pk_bf16_f32 v194, v48, v49
	v_cvt_pk_bf16_f32 v195, v50, v51
	global_store_dwordx4 v[158:159], v[192:195], off offset:256
	v_pk_add_f32 v[44:45], v[44:45], v[172:173]
	v_pk_add_f32 v[46:47], v[46:47], v[174:175]
	v_pk_add_f32 v[40:41], v[40:41], v[176:177]
	v_pk_add_f32 v[42:43], v[42:43], v[178:179]
	v_pk_mul_f32 v[44:45], v[44:45], v[196:197]
	v_pk_mul_f32 v[46:47], v[46:47], v[196:197]
	v_pk_mul_f32 v[40:41], v[40:41], v[196:197]
	v_pk_mul_f32 v[42:43], v[42:43], v[196:197]
	v_exp_f32_e32 v44, v44
	v_exp_f32_e32 v45, v45
	v_exp_f32_e32 v46, v46
	v_exp_f32_e32 v47, v47
	v_exp_f32_e32 v40, v40
	v_exp_f32_e32 v41, v41
	v_exp_f32_e32 v42, v42
	v_exp_f32_e32 v43, v43
	v_pk_add_f32 v[44:45], v[44:45], 1.0 op_sel_hi:[1,0]
	v_pk_add_f32 v[46:47], v[46:47], 1.0 op_sel_hi:[1,0]
	v_pk_add_f32 v[40:41], v[40:41], 1.0 op_sel_hi:[1,0]
	v_pk_add_f32 v[42:43], v[42:43], 1.0 op_sel_hi:[1,0]
	v_div_scale_f32 v180, s[100:101], v44, v44, 1.0
	v_rcp_f32_e32 v181, v180
	v_div_scale_f32 v182, vcc, 1.0, v44, 1.0
	v_fma_f32 v183, -v180, v181, 1.0
	v_fmac_f32_e32 v181, v183, v181
	v_mul_f32_e32 v183, v182, v181
	v_fma_f32 v184, -v180, v183, v182
	v_fmac_f32_e32 v183, v184, v181
	v_fma_f32 v180, -v180, v183, v182
	v_div_fmas_f32 v180, v180, v181, v183
	v_div_fixup_f32 v44, v180, v44, 1.0
	v_div_scale_f32 v180, s[100:101], v45, v45, 1.0
	v_rcp_f32_e32 v181, v180
	v_div_scale_f32 v182, vcc, 1.0, v45, 1.0
	v_fma_f32 v183, -v180, v181, 1.0
	v_fmac_f32_e32 v181, v183, v181
	v_mul_f32_e32 v183, v182, v181
	v_fma_f32 v184, -v180, v183, v182
	v_fmac_f32_e32 v183, v184, v181
	v_fma_f32 v180, -v180, v183, v182
	v_div_fmas_f32 v180, v180, v181, v183
	v_div_fixup_f32 v45, v180, v45, 1.0
	v_div_scale_f32 v180, s[100:101], v46, v46, 1.0
	v_rcp_f32_e32 v181, v180
	v_div_scale_f32 v182, vcc, 1.0, v46, 1.0
	v_fma_f32 v183, -v180, v181, 1.0
	v_fmac_f32_e32 v181, v183, v181
	v_mul_f32_e32 v183, v182, v181
	v_fma_f32 v184, -v180, v183, v182
	v_fmac_f32_e32 v183, v184, v181
	v_fma_f32 v180, -v180, v183, v182
	v_div_fmas_f32 v180, v180, v181, v183
	v_div_fixup_f32 v46, v180, v46, 1.0
	v_div_scale_f32 v180, s[100:101], v47, v47, 1.0
	v_rcp_f32_e32 v181, v180
	v_div_scale_f32 v182, vcc, 1.0, v47, 1.0
	v_fma_f32 v183, -v180, v181, 1.0
	v_fmac_f32_e32 v181, v183, v181
	v_mul_f32_e32 v183, v182, v181
	v_fma_f32 v184, -v180, v183, v182
	v_fmac_f32_e32 v183, v184, v181
	v_fma_f32 v180, -v180, v183, v182
	v_div_fmas_f32 v180, v180, v181, v183
	v_div_fixup_f32 v47, v180, v47, 1.0
	v_div_scale_f32 v180, s[100:101], v40, v40, 1.0
	v_rcp_f32_e32 v181, v180
	v_div_scale_f32 v182, vcc, 1.0, v40, 1.0
	v_fma_f32 v183, -v180, v181, 1.0
	v_fmac_f32_e32 v181, v183, v181
	v_mul_f32_e32 v183, v182, v181
	v_fma_f32 v184, -v180, v183, v182
	v_fmac_f32_e32 v183, v184, v181
	v_fma_f32 v180, -v180, v183, v182
	v_div_fmas_f32 v180, v180, v181, v183
	v_div_fixup_f32 v40, v180, v40, 1.0
	v_div_scale_f32 v180, s[100:101], v41, v41, 1.0
	v_rcp_f32_e32 v181, v180
	v_div_scale_f32 v182, vcc, 1.0, v41, 1.0
	v_fma_f32 v183, -v180, v181, 1.0
	v_fmac_f32_e32 v181, v183, v181
	v_mul_f32_e32 v183, v182, v181
	v_fma_f32 v184, -v180, v183, v182
	v_fmac_f32_e32 v183, v184, v181
	v_fma_f32 v180, -v180, v183, v182
	v_div_fmas_f32 v180, v180, v181, v183
	v_div_fixup_f32 v41, v180, v41, 1.0
	v_div_scale_f32 v180, s[100:101], v42, v42, 1.0
	v_rcp_f32_e32 v181, v180
	v_div_scale_f32 v182, vcc, 1.0, v42, 1.0
	v_fma_f32 v183, -v180, v181, 1.0
	v_fmac_f32_e32 v181, v183, v181
	v_mul_f32_e32 v183, v182, v181
	v_fma_f32 v184, -v180, v183, v182
	v_fmac_f32_e32 v183, v184, v181
	v_fma_f32 v180, -v180, v183, v182
	v_div_fmas_f32 v180, v180, v181, v183
	v_div_fixup_f32 v42, v180, v42, 1.0
	v_div_scale_f32 v180, s[100:101], v43, v43, 1.0
	v_rcp_f32_e32 v181, v180
	v_div_scale_f32 v182, vcc, 1.0, v43, 1.0
	v_fma_f32 v183, -v180, v181, 1.0
	v_fmac_f32_e32 v181, v183, v181
	v_mul_f32_e32 v183, v182, v181
	v_fma_f32 v184, -v180, v183, v182
	v_fmac_f32_e32 v183, v184, v181
	v_fma_f32 v180, -v180, v183, v182
	v_div_fmas_f32 v180, v180, v181, v183
	v_div_fixup_f32 v43, v180, v43, 1.0
	v_pk_mul_f32 v[44:45], v[44:45], v[198:199]
	v_pk_mul_f32 v[46:47], v[46:47], v[198:199]
	v_pk_mul_f32 v[40:41], v[40:41], v[198:199]
	v_pk_mul_f32 v[42:43], v[42:43], v[198:199]
	s_mov_b64 s[98:99], 0x8000
	v_lshl_add_u64 v[158:159], v[156:157], 0, s[98:99]
	v_cvt_pk_bf16_f32 v188, v44, v45
	v_cvt_pk_bf16_f32 v189, v46, v47
	v_cvt_pk_bf16_f32 v190, v40, v41
	v_cvt_pk_bf16_f32 v191, v42, v43
	global_store_dwordx4 v[158:159], v[188:191], off offset:256
	v_pk_add_f32 v[36:37], v[36:37], v[172:173]
	v_pk_add_f32 v[38:39], v[38:39], v[174:175]
	v_pk_add_f32 v[32:33], v[32:33], v[176:177]
	v_pk_add_f32 v[34:35], v[34:35], v[178:179]
	v_pk_mul_f32 v[36:37], v[36:37], v[196:197]
	v_pk_mul_f32 v[38:39], v[38:39], v[196:197]
	v_pk_mul_f32 v[32:33], v[32:33], v[196:197]
	v_pk_mul_f32 v[34:35], v[34:35], v[196:197]
	v_exp_f32_e32 v36, v36
	v_exp_f32_e32 v37, v37
	v_exp_f32_e32 v38, v38
	v_exp_f32_e32 v39, v39
	v_exp_f32_e32 v32, v32
	v_exp_f32_e32 v33, v33
	v_exp_f32_e32 v34, v34
	v_exp_f32_e32 v35, v35
	v_pk_add_f32 v[36:37], v[36:37], 1.0 op_sel_hi:[1,0]
	v_pk_add_f32 v[38:39], v[38:39], 1.0 op_sel_hi:[1,0]
	v_pk_add_f32 v[32:33], v[32:33], 1.0 op_sel_hi:[1,0]
	v_pk_add_f32 v[34:35], v[34:35], 1.0 op_sel_hi:[1,0]
	v_div_scale_f32 v180, s[100:101], v36, v36, 1.0
	v_rcp_f32_e32 v181, v180
	v_div_scale_f32 v182, vcc, 1.0, v36, 1.0
	v_fma_f32 v183, -v180, v181, 1.0
	v_fmac_f32_e32 v181, v183, v181
	v_mul_f32_e32 v183, v182, v181
	v_fma_f32 v184, -v180, v183, v182
	v_fmac_f32_e32 v183, v184, v181
	v_fma_f32 v180, -v180, v183, v182
	v_div_fmas_f32 v180, v180, v181, v183
; __device__ __forceinline__ unsigned cvt_pk_bf16(float lo, float hi) { const f32x2c v = {lo, hi}; const bf16x2c b = __builtin_convertvector(v, bf16x2c); return __builtin_bit_cast(unsigned, b); }
; __device__ __forceinline__ float sigmoidf_(float x) { return 1.f / (1.f + __expf(-x)); }
;     __device__ __forceinline__ void operator()(const f32x4 (&acc)[2][2][4][2], const Unit& u, int wr, int wc, int fr, int fq) const {
;     ...
;                     const f32x4 v0 = acc[ai][bj][m][0] + b0, v1 = acc[ai][bj][m][1] + b1; float o[8];
; #pragma unroll
;                     for (int e = 0; e < 8; ++e) { float x = (e < 4) ? v0[e & 3] : v1[e & 3];
;                         if (kind == 0) x = -0.6065306597126334f * sigmoidf_(x);
;                         else if (kind == 1) x = sigmoidf_(x);
;                         o[e] = x; }
;                     u32x4 w; w.x = cvt_pk_bf16(o[0], o[1]); w.y = cvt_pk_bf16(o[2], o[3]); w.z = cvt_pk_bf16(o[4], o[5]); w.w = cvt_pk_bf16(o[6], o[7]);
;                     *(u32x4*)(O + row * 512 + col) = w; } }
	v_div_fixup_f32 v36, v180, v36, 1.0
	v_div_scale_f32 v180, s[100:101], v37, v37, 1.0
	v_rcp_f32_e32 v181, v180
	v_div_scale_f32 v182, vcc, 1.0, v37, 1.0
	v_fma_f32 v183, -v180, v181, 1.0
	v_fmac_f32_e32 v181, v183, v181
	v_mul_f32_e32 v183, v182, v181
	v_fma_f32 v184, -v180, v183, v182
	v_fmac_f32_e32 v183, v184, v181
	v_fma_f32 v180, -v180, v183, v182
	v_div_fmas_f32 v180, v180, v181, v183
	v_div_fixup_f32 v37, v180, v37, 1.0
	v_div_scale_f32 v180, s[100:101], v38, v38, 1.0
	v_rcp_f32_e32 v181, v180
	v_div_scale_f32 v182, vcc, 1.0, v38, 1.0
	v_fma_f32 v183, -v180, v181, 1.0
	v_fmac_f32_e32 v181, v183, v181
	v_mul_f32_e32 v183, v182, v181
	v_fma_f32 v184, -v180, v183, v182
	v_fmac_f32_e32 v183, v184, v181
	v_fma_f32 v180, -v180, v183, v182
	v_div_fmas_f32 v180, v180, v181, v183
	v_div_fixup_f32 v38, v180, v38, 1.0
	v_div_scale_f32 v180, s[100:101], v39, v39, 1.0
	v_rcp_f32_e32 v181, v180
	v_div_scale_f32 v182, vcc, 1.0, v39, 1.0
	v_fma_f32 v183, -v180, v181, 1.0
	v_fmac_f32_e32 v181, v183, v181
	v_mul_f32_e32 v183, v182, v181
	v_fma_f32 v184, -v180, v183, v182
	v_fmac_f32_e32 v183, v184, v181
	v_fma_f32 v180, -v180, v183, v182
	v_div_fmas_f32 v180, v180, v181, v183
	v_div_fixup_f32 v39, v180, v39, 1.0
	v_div_scale_f32 v180, s[100:101], v32, v32, 1.0
	v_rcp_f32_e32 v181, v180
	v_div_scale_f32 v182, vcc, 1.0, v32, 1.0
	v_fma_f32 v183, -v180, v181, 1.0
	v_fmac_f32_e32 v181, v183, v181
	v_mul_f32_e32 v183, v182, v181
	v_fma_f32 v184, -v180, v183, v182
	v_fmac_f32_e32 v183, v184, v181
	v_fma_f32 v180, -v180, v183, v182
	v_div_fmas_f32 v180, v180, v181, v183
	v_div_fixup_f32 v32, v180, v32, 1.0
	v_div_scale_f32 v180, s[100:101], v33, v33, 1.0
	v_rcp_f32_e32 v181, v180
	v_div_scale_f32 v182, vcc, 1.0, v33, 1.0
	v_fma_f32 v183, -v180, v181, 1.0
	v_fmac_f32_e32 v181, v183, v181
	v_mul_f32_e32 v183, v182, v181
	v_fma_f32 v184, -v180, v183, v182
	v_fmac_f32_e32 v183, v184, v181
	v_fma_f32 v180, -v180, v183, v182
	v_div_fmas_f32 v180, v180, v181, v183
	v_div_fixup_f32 v33, v180, v33, 1.0
	v_div_scale_f32 v180, s[100:101], v34, v34, 1.0
	v_rcp_f32_e32 v181, v180
	v_div_scale_f32 v182, vcc, 1.0, v34, 1.0
	v_fma_f32 v183, -v180, v181, 1.0
	v_fmac_f32_e32 v181, v183, v181
	v_mul_f32_e32 v183, v182, v181
	v_fma_f32 v184, -v180, v183, v182
	v_fmac_f32_e32 v183, v184, v181
	v_fma_f32 v180, -v180, v183, v182
	v_div_fmas_f32 v180, v180, v181, v183
	v_div_fixup_f32 v34, v180, v34, 1.0
	v_div_scale_f32 v180, s[100:101], v35, v35, 1.0
	v_rcp_f32_e32 v181, v180
	v_div_scale_f32 v182, vcc, 1.0, v35, 1.0
	v_fma_f32 v183, -v180, v181, 1.0
	v_fmac_f32_e32 v181, v183, v181
	v_mul_f32_e32 v183, v182, v181
	v_fma_f32 v184, -v180, v183, v182
	v_fmac_f32_e32 v183, v184, v181
	v_fma_f32 v180, -v180, v183, v182
	v_div_fmas_f32 v180, v180, v181, v183
	v_div_fixup_f32 v35, v180, v35, 1.0
	v_pk_mul_f32 v[36:37], v[36:37], v[198:199]
	v_pk_mul_f32 v[38:39], v[38:39], v[198:199]
	v_pk_mul_f32 v[32:33], v[32:33], v[198:199]
	v_pk_mul_f32 v[34:35], v[34:35], v[198:199]
	s_mov_b64 s[98:99], 0xc000
	v_lshl_add_u64 v[158:159], v[156:157], 0, s[98:99]
	v_cvt_pk_bf16_f32 v192, v36, v37
	v_cvt_pk_bf16_f32 v193, v38, v39
	v_cvt_pk_bf16_f32 v194, v32, v33
	v_cvt_pk_bf16_f32 v195, v34, v35
	global_store_dwordx4 v[158:159], v[192:195], off offset:256
	v_pk_add_f32 v[28:29], v[28:29], v[172:173]
	v_pk_add_f32 v[30:31], v[30:31], v[174:175]
	v_pk_add_f32 v[24:25], v[24:25], v[176:177]
	v_pk_add_f32 v[26:27], v[26:27], v[178:179]
	v_pk_mul_f32 v[28:29], v[28:29], v[196:197]
	v_pk_mul_f32 v[30:31], v[30:31], v[196:197]
	v_pk_mul_f32 v[24:25], v[24:25], v[196:197]
	v_pk_mul_f32 v[26:27], v[26:27], v[196:197]
	v_exp_f32_e32 v28, v28
	v_exp_f32_e32 v29, v29
	v_exp_f32_e32 v30, v30
	v_exp_f32_e32 v31, v31
	v_exp_f32_e32 v24, v24
	v_exp_f32_e32 v25, v25
	v_exp_f32_e32 v26, v26
	v_exp_f32_e32 v27, v27
	v_pk_add_f32 v[28:29], v[28:29], 1.0 op_sel_hi:[1,0]
	v_pk_add_f32 v[30:31], v[30:31], 1.0 op_sel_hi:[1,0]
	v_pk_add_f32 v[24:25], v[24:25], 1.0 op_sel_hi:[1,0]
	v_pk_add_f32 v[26:27], v[26:27], 1.0 op_sel_hi:[1,0]
	v_div_scale_f32 v180, s[100:101], v28, v28, 1.0
	v_rcp_f32_e32 v181, v180
	v_div_scale_f32 v182, vcc, 1.0, v28, 1.0
	v_fma_f32 v183, -v180, v181, 1.0
	v_fmac_f32_e32 v181, v183, v181
	v_mul_f32_e32 v183, v182, v181
	v_fma_f32 v184, -v180, v183, v182
	v_fmac_f32_e32 v183, v184, v181
	v_fma_f32 v180, -v180, v183, v182
	v_div_fmas_f32 v180, v180, v181, v183
	v_div_fixup_f32 v28, v180, v28, 1.0
	v_div_scale_f32 v180, s[100:101], v29, v29, 1.0
	v_rcp_f32_e32 v181, v180
	v_div_scale_f32 v182, vcc, 1.0, v29, 1.0
	v_fma_f32 v183, -v180, v181, 1.0
	v_fmac_f32_e32 v181, v183, v181
	v_mul_f32_e32 v183, v182, v181
	v_fma_f32 v184, -v180, v183, v182
	v_fmac_f32_e32 v183, v184, v181
	v_fma_f32 v180, -v180, v183, v182
	v_div_fmas_f32 v180, v180, v181, v183
	v_div_fixup_f32 v29, v180, v29, 1.0
	v_div_scale_f32 v180, s[100:101], v30, v30, 1.0
	v_rcp_f32_e32 v181, v180
	v_div_scale_f32 v182, vcc, 1.0, v30, 1.0
	v_fma_f32 v183, -v180, v181, 1.0
	v_fmac_f32_e32 v181, v183, v181
	v_mul_f32_e32 v183, v182, v181
	v_fma_f32 v184, -v180, v183, v182
	v_fmac_f32_e32 v183, v184, v181
	v_fma_f32 v180, -v180, v183, v182
	v_div_fmas_f32 v180, v180, v181, v183
	v_div_fixup_f32 v30, v180, v30, 1.0
	v_div_scale_f32 v180, s[100:101], v31, v31, 1.0
	v_rcp_f32_e32 v181, v180
	v_div_scale_f32 v182, vcc, 1.0, v31, 1.0
	v_fma_f32 v183, -v180, v181, 1.0
	v_fmac_f32_e32 v181, v183, v181
	v_mul_f32_e32 v183, v182, v181
	v_fma_f32 v184, -v180, v183, v182
	v_fmac_f32_e32 v183, v184, v181
	v_fma_f32 v180, -v180, v183, v182
	v_div_fmas_f32 v180, v180, v181, v183
	v_div_fixup_f32 v31, v180, v31, 1.0
	v_div_scale_f32 v180, s[100:101], v24, v24, 1.0
; __device__ __forceinline__ unsigned cvt_pk_bf16(float lo, float hi) { const f32x2c v = {lo, hi}; const bf16x2c b = __builtin_convertvector(v, bf16x2c); return __builtin_bit_cast(unsigned, b); }
; __device__ __forceinline__ float sigmoidf_(float x) { return 1.f / (1.f + __expf(-x)); }
;     __device__ __forceinline__ void operator()(const f32x4 (&acc)[2][2][4][2], const Unit& u, int wr, int wc, int fr, int fq) const {
;     ...
;                     const f32x4 v0 = acc[ai][bj][m][0] + b0, v1 = acc[ai][bj][m][1] + b1; float o[8];
; #pragma unroll
;                     for (int e = 0; e < 8; ++e) { float x = (e < 4) ? v0[e & 3] : v1[e & 3];
;                         if (kind == 0) x = -0.6065306597126334f * sigmoidf_(x);
;                         else if (kind == 1) x = sigmoidf_(x);
;                         o[e] = x; }
;                     u32x4 w; w.x = cvt_pk_bf16(o[0], o[1]); w.y = cvt_pk_bf16(o[2], o[3]); w.z = cvt_pk_bf16(o[4], o[5]); w.w = cvt_pk_bf16(o[6], o[7]);
;                     *(u32x4*)(O + row * 512 + col) = w; } }
	v_rcp_f32_e32 v181, v180
	v_div_scale_f32 v182, vcc, 1.0, v24, 1.0
	v_fma_f32 v183, -v180, v181, 1.0
	v_fmac_f32_e32 v181, v183, v181
	v_mul_f32_e32 v183, v182, v181
	v_fma_f32 v184, -v180, v183, v182
	v_fmac_f32_e32 v183, v184, v181
	v_fma_f32 v180, -v180, v183, v182
	v_div_fmas_f32 v180, v180, v181, v183
	v_div_fixup_f32 v24, v180, v24, 1.0
	v_div_scale_f32 v180, s[100:101], v25, v25, 1.0
	v_rcp_f32_e32 v181, v180
	v_div_scale_f32 v182, vcc, 1.0, v25, 1.0
	v_fma_f32 v183, -v180, v181, 1.0
	v_fmac_f32_e32 v181, v183, v181
	v_mul_f32_e32 v183, v182, v181
	v_fma_f32 v184, -v180, v183, v182
	v_fmac_f32_e32 v183, v184, v181
	v_fma_f32 v180, -v180, v183, v182
	v_div_fmas_f32 v180, v180, v181, v183
	v_div_fixup_f32 v25, v180, v25, 1.0
	v_div_scale_f32 v180, s[100:101], v26, v26, 1.0
	v_rcp_f32_e32 v181, v180
	v_div_scale_f32 v182, vcc, 1.0, v26, 1.0
	v_fma_f32 v183, -v180, v181, 1.0
	v_fmac_f32_e32 v181, v183, v181
	v_mul_f32_e32 v183, v182, v181
	v_fma_f32 v184, -v180, v183, v182
	v_fmac_f32_e32 v183, v184, v181
	v_fma_f32 v180, -v180, v183, v182
	v_div_fmas_f32 v180, v180, v181, v183
	v_div_fixup_f32 v26, v180, v26, 1.0
	v_div_scale_f32 v180, s[100:101], v27, v27, 1.0
	v_rcp_f32_e32 v181, v180
	v_div_scale_f32 v182, vcc, 1.0, v27, 1.0
	v_fma_f32 v183, -v180, v181, 1.0
	v_fmac_f32_e32 v181, v183, v181
	v_mul_f32_e32 v183, v182, v181
	v_fma_f32 v184, -v180, v183, v182
	v_fmac_f32_e32 v183, v184, v181
	v_fma_f32 v180, -v180, v183, v182
	v_div_fmas_f32 v180, v180, v181, v183
	v_div_fixup_f32 v27, v180, v27, 1.0
	v_pk_mul_f32 v[28:29], v[28:29], v[198:199]
	v_pk_mul_f32 v[30:31], v[30:31], v[198:199]
	v_pk_mul_f32 v[24:25], v[24:25], v[198:199]
	v_pk_mul_f32 v[26:27], v[26:27], v[198:199]
	s_mov_b64 s[98:99], 0x20000
	v_lshl_add_u64 v[158:159], v[156:157], 0, s[98:99]
	v_cvt_pk_bf16_f32 v188, v28, v29
	v_cvt_pk_bf16_f32 v189, v30, v31
	v_cvt_pk_bf16_f32 v190, v24, v25
	v_cvt_pk_bf16_f32 v191, v26, v27
	global_store_dwordx4 v[158:159], v[188:191], off offset:256
	v_pk_add_f32 v[20:21], v[20:21], v[172:173]
	v_pk_add_f32 v[22:23], v[22:23], v[174:175]
	v_pk_add_f32 v[16:17], v[16:17], v[176:177]
	v_pk_add_f32 v[18:19], v[18:19], v[178:179]
	v_pk_mul_f32 v[20:21], v[20:21], v[196:197]
	v_pk_mul_f32 v[22:23], v[22:23], v[196:197]
	v_pk_mul_f32 v[16:17], v[16:17], v[196:197]
	v_pk_mul_f32 v[18:19], v[18:19], v[196:197]
	v_exp_f32_e32 v20, v20
	v_exp_f32_e32 v21, v21
	v_exp_f32_e32 v22, v22
	v_exp_f32_e32 v23, v23
	v_exp_f32_e32 v16, v16
	v_exp_f32_e32 v17, v17
	v_exp_f32_e32 v18, v18
	v_exp_f32_e32 v19, v19
	v_pk_add_f32 v[20:21], v[20:21], 1.0 op_sel_hi:[1,0]
	v_pk_add_f32 v[22:23], v[22:23], 1.0 op_sel_hi:[1,0]
	v_pk_add_f32 v[16:17], v[16:17], 1.0 op_sel_hi:[1,0]
	v_pk_add_f32 v[18:19], v[18:19], 1.0 op_sel_hi:[1,0]
	v_div_scale_f32 v180, s[100:101], v20, v20, 1.0
	v_rcp_f32_e32 v181, v180
	v_div_scale_f32 v182, vcc, 1.0, v20, 1.0
	v_fma_f32 v183, -v180, v181, 1.0
	v_fmac_f32_e32 v181, v183, v181
	v_mul_f32_e32 v183, v182, v181
	v_fma_f32 v184, -v180, v183, v182
	v_fmac_f32_e32 v183, v184, v181
	v_fma_f32 v180, -v180, v183, v182
	v_div_fmas_f32 v180, v180, v181, v183
	v_div_fixup_f32 v20, v180, v20, 1.0
	v_div_scale_f32 v180, s[100:101], v21, v21, 1.0
	v_rcp_f32_e32 v181, v180
	v_div_scale_f32 v182, vcc, 1.0, v21, 1.0
	v_fma_f32 v183, -v180, v181, 1.0
	v_fmac_f32_e32 v181, v183, v181
	v_mul_f32_e32 v183, v182, v181
	v_fma_f32 v184, -v180, v183, v182
	v_fmac_f32_e32 v183, v184, v181
	v_fma_f32 v180, -v180, v183, v182
	v_div_fmas_f32 v180, v180, v181, v183
	v_div_fixup_f32 v21, v180, v21, 1.0
	v_div_scale_f32 v180, s[100:101], v22, v22, 1.0
	v_rcp_f32_e32 v181, v180
	v_div_scale_f32 v182, vcc, 1.0, v22, 1.0
	v_fma_f32 v183, -v180, v181, 1.0
	v_fmac_f32_e32 v181, v183, v181
	v_mul_f32_e32 v183, v182, v181
	v_fma_f32 v184, -v180, v183, v182
	v_fmac_f32_e32 v183, v184, v181
	v_fma_f32 v180, -v180, v183, v182
	v_div_fmas_f32 v180, v180, v181, v183
	v_div_fixup_f32 v22, v180, v22, 1.0
	v_div_scale_f32 v180, s[100:101], v23, v23, 1.0
	v_rcp_f32_e32 v181, v180
	v_div_scale_f32 v182, vcc, 1.0, v23, 1.0
	v_fma_f32 v183, -v180, v181, 1.0
	v_fmac_f32_e32 v181, v183, v181
	v_mul_f32_e32 v183, v182, v181
	v_fma_f32 v184, -v180, v183, v182
	v_fmac_f32_e32 v183, v184, v181
	v_fma_f32 v180, -v180, v183, v182
	v_div_fmas_f32 v180, v180, v181, v183
	v_div_fixup_f32 v23, v180, v23, 1.0
	v_div_scale_f32 v180, s[100:101], v16, v16, 1.0
	v_rcp_f32_e32 v181, v180
	v_div_scale_f32 v182, vcc, 1.0, v16, 1.0
	v_fma_f32 v183, -v180, v181, 1.0
	v_fmac_f32_e32 v181, v183, v181
	v_mul_f32_e32 v183, v182, v181
	v_fma_f32 v184, -v180, v183, v182
	v_fmac_f32_e32 v183, v184, v181
	v_fma_f32 v180, -v180, v183, v182
	v_div_fmas_f32 v180, v180, v181, v183
	v_div_fixup_f32 v16, v180, v16, 1.0
	v_div_scale_f32 v180, s[100:101], v17, v17, 1.0
	v_rcp_f32_e32 v181, v180
	v_div_scale_f32 v182, vcc, 1.0, v17, 1.0
	v_fma_f32 v183, -v180, v181, 1.0
	v_fmac_f32_e32 v181, v183, v181
	v_mul_f32_e32 v183, v182, v181
	v_fma_f32 v184, -v180, v183, v182
	v_fmac_f32_e32 v183, v184, v181
	v_fma_f32 v180, -v180, v183, v182
	v_div_fmas_f32 v180, v180, v181, v183
	v_div_fixup_f32 v17, v180, v17, 1.0
	v_div_scale_f32 v180, s[100:101], v18, v18, 1.0
	v_rcp_f32_e32 v181, v180
	v_div_scale_f32 v182, vcc, 1.0, v18, 1.0
	v_fma_f32 v183, -v180, v181, 1.0
	v_fmac_f32_e32 v181, v183, v181
	v_mul_f32_e32 v183, v182, v181
	v_fma_f32 v184, -v180, v183, v182
	v_fmac_f32_e32 v183, v184, v181
	v_fma_f32 v180, -v180, v183, v182
	v_div_fmas_f32 v180, v180, v181, v183
	v_div_fixup_f32 v18, v180, v18, 1.0
	v_div_scale_f32 v180, s[100:101], v19, v19, 1.0
	v_rcp_f32_e32 v181, v180
	v_div_scale_f32 v182, vcc, 1.0, v19, 1.0
; __device__ __forceinline__ unsigned cvt_pk_bf16(float lo, float hi) { const f32x2c v = {lo, hi}; const bf16x2c b = __builtin_convertvector(v, bf16x2c); return __builtin_bit_cast(unsigned, b); }
; __device__ __forceinline__ float sigmoidf_(float x) { return 1.f / (1.f + __expf(-x)); }
;     __device__ __forceinline__ void operator()(const f32x4 (&acc)[2][2][4][2], const Unit& u, int wr, int wc, int fr, int fq) const {
;     ...
;                     const f32x4 v0 = acc[ai][bj][m][0] + b0, v1 = acc[ai][bj][m][1] + b1; float o[8];
; #pragma unroll
;                     for (int e = 0; e < 8; ++e) { float x = (e < 4) ? v0[e & 3] : v1[e & 3];
;                         if (kind == 0) x = -0.6065306597126334f * sigmoidf_(x);
;                         else if (kind == 1) x = sigmoidf_(x);
;                         o[e] = x; }
;                     u32x4 w; w.x = cvt_pk_bf16(o[0], o[1]); w.y = cvt_pk_bf16(o[2], o[3]); w.z = cvt_pk_bf16(o[4], o[5]); w.w = cvt_pk_bf16(o[6], o[7]);
;                     *(u32x4*)(O + row * 512 + col) = w; } }
	v_fma_f32 v183, -v180, v181, 1.0
	v_fmac_f32_e32 v181, v183, v181
	v_mul_f32_e32 v183, v182, v181
	v_fma_f32 v184, -v180, v183, v182
	v_fmac_f32_e32 v183, v184, v181
	v_fma_f32 v180, -v180, v183, v182
	v_div_fmas_f32 v180, v180, v181, v183
	v_div_fixup_f32 v19, v180, v19, 1.0
	v_pk_mul_f32 v[20:21], v[20:21], v[198:199]
	v_pk_mul_f32 v[22:23], v[22:23], v[198:199]
	v_pk_mul_f32 v[16:17], v[16:17], v[198:199]
	v_pk_mul_f32 v[18:19], v[18:19], v[198:199]
	s_mov_b64 s[98:99], 0x24000
	v_lshl_add_u64 v[158:159], v[156:157], 0, s[98:99]
	v_cvt_pk_bf16_f32 v192, v20, v21
	v_cvt_pk_bf16_f32 v193, v22, v23
	v_cvt_pk_bf16_f32 v194, v16, v17
	v_cvt_pk_bf16_f32 v195, v18, v19
	global_store_dwordx4 v[158:159], v[192:195], off offset:256
	v_pk_add_f32 v[12:13], v[12:13], v[172:173]
	v_pk_add_f32 v[14:15], v[14:15], v[174:175]
	v_pk_add_f32 v[8:9], v[8:9], v[176:177]
	v_pk_add_f32 v[10:11], v[10:11], v[178:179]
	v_pk_mul_f32 v[12:13], v[12:13], v[196:197]
	v_pk_mul_f32 v[14:15], v[14:15], v[196:197]
	v_pk_mul_f32 v[8:9], v[8:9], v[196:197]
	v_pk_mul_f32 v[10:11], v[10:11], v[196:197]
	v_exp_f32_e32 v12, v12
	v_exp_f32_e32 v13, v13
	v_exp_f32_e32 v14, v14
	v_exp_f32_e32 v15, v15
	v_exp_f32_e32 v8, v8
	v_exp_f32_e32 v9, v9
	v_exp_f32_e32 v10, v10
	v_exp_f32_e32 v11, v11
	v_pk_add_f32 v[12:13], v[12:13], 1.0 op_sel_hi:[1,0]
	v_pk_add_f32 v[14:15], v[14:15], 1.0 op_sel_hi:[1,0]
	v_pk_add_f32 v[8:9], v[8:9], 1.0 op_sel_hi:[1,0]
	v_pk_add_f32 v[10:11], v[10:11], 1.0 op_sel_hi:[1,0]
	v_div_scale_f32 v180, s[100:101], v12, v12, 1.0
	v_rcp_f32_e32 v181, v180
	v_div_scale_f32 v182, vcc, 1.0, v12, 1.0
	v_fma_f32 v183, -v180, v181, 1.0
	v_fmac_f32_e32 v181, v183, v181
	v_mul_f32_e32 v183, v182, v181
	v_fma_f32 v184, -v180, v183, v182
	v_fmac_f32_e32 v183, v184, v181
	v_fma_f32 v180, -v180, v183, v182
	v_div_fmas_f32 v180, v180, v181, v183
	v_div_fixup_f32 v12, v180, v12, 1.0
	v_div_scale_f32 v180, s[100:101], v13, v13, 1.0
	v_rcp_f32_e32 v181, v180
	v_div_scale_f32 v182, vcc, 1.0, v13, 1.0
	v_fma_f32 v183, -v180, v181, 1.0
	v_fmac_f32_e32 v181, v183, v181
	v_mul_f32_e32 v183, v182, v181
	v_fma_f32 v184, -v180, v183, v182
	v_fmac_f32_e32 v183, v184, v181
	v_fma_f32 v180, -v180, v183, v182
	v_div_fmas_f32 v180, v180, v181, v183
	v_div_fixup_f32 v13, v180, v13, 1.0
	v_div_scale_f32 v180, s[100:101], v14, v14, 1.0
	v_rcp_f32_e32 v181, v180
	v_div_scale_f32 v182, vcc, 1.0, v14, 1.0
	v_fma_f32 v183, -v180, v181, 1.0
	v_fmac_f32_e32 v181, v183, v181
	v_mul_f32_e32 v183, v182, v181
	v_fma_f32 v184, -v180, v183, v182
	v_fmac_f32_e32 v183, v184, v181
	v_fma_f32 v180, -v180, v183, v182
	v_div_fmas_f32 v180, v180, v181, v183
	v_div_fixup_f32 v14, v180, v14, 1.0
	v_div_scale_f32 v180, s[100:101], v15, v15, 1.0
	v_rcp_f32_e32 v181, v180
	v_div_scale_f32 v182, vcc, 1.0, v15, 1.0
	v_fma_f32 v183, -v180, v181, 1.0
	v_fmac_f32_e32 v181, v183, v181
	v_mul_f32_e32 v183, v182, v181
	v_fma_f32 v184, -v180, v183, v182
	v_fmac_f32_e32 v183, v184, v181
	v_fma_f32 v180, -v180, v183, v182
	v_div_fmas_f32 v180, v180, v181, v183
	v_div_fixup_f32 v15, v180, v15, 1.0
	v_div_scale_f32 v180, s[100:101], v8, v8, 1.0
	v_rcp_f32_e32 v181, v180
	v_div_scale_f32 v182, vcc, 1.0, v8, 1.0
	v_fma_f32 v183, -v180, v181, 1.0
	v_fmac_f32_e32 v181, v183, v181
	v_mul_f32_e32 v183, v182, v181
	v_fma_f32 v184, -v180, v183, v182
	v_fmac_f32_e32 v183, v184, v181
	v_fma_f32 v180, -v180, v183, v182
	v_div_fmas_f32 v180, v180, v181, v183
	v_div_fixup_f32 v8, v180, v8, 1.0
	v_div_scale_f32 v180, s[100:101], v9, v9, 1.0
	v_rcp_f32_e32 v181, v180
	v_div_scale_f32 v182, vcc, 1.0, v9, 1.0
	v_fma_f32 v183, -v180, v181, 1.0
	v_fmac_f32_e32 v181, v183, v181
	v_mul_f32_e32 v183, v182, v181
	v_fma_f32 v184, -v180, v183, v182
	v_fmac_f32_e32 v183, v184, v181
	v_fma_f32 v180, -v180, v183, v182
	v_div_fmas_f32 v180, v180, v181, v183
	v_div_fixup_f32 v9, v180, v9, 1.0
	v_div_scale_f32 v180, s[100:101], v10, v10, 1.0
	v_rcp_f32_e32 v181, v180
	v_div_scale_f32 v182, vcc, 1.0, v10, 1.0
	v_fma_f32 v183, -v180, v181, 1.0
	v_fmac_f32_e32 v181, v183, v181
	v_mul_f32_e32 v183, v182, v181
	v_fma_f32 v184, -v180, v183, v182
	v_fmac_f32_e32 v183, v184, v181
	v_fma_f32 v180, -v180, v183, v182
	v_div_fmas_f32 v180, v180, v181, v183
	v_div_fixup_f32 v10, v180, v10, 1.0
	v_div_scale_f32 v180, s[100:101], v11, v11, 1.0
	v_rcp_f32_e32 v181, v180
	v_div_scale_f32 v182, vcc, 1.0, v11, 1.0
	v_fma_f32 v183, -v180, v181, 1.0
	v_fmac_f32_e32 v181, v183, v181
	v_mul_f32_e32 v183, v182, v181
	v_fma_f32 v184, -v180, v183, v182
	v_fmac_f32_e32 v183, v184, v181
	v_fma_f32 v180, -v180, v183, v182
	v_div_fmas_f32 v180, v180, v181, v183
	v_div_fixup_f32 v11, v180, v11, 1.0
	v_pk_mul_f32 v[12:13], v[12:13], v[198:199]
; __device__ __forceinline__ unsigned cvt_pk_bf16(float lo, float hi) { const f32x2c v = {lo, hi}; const bf16x2c b = __builtin_convertvector(v, bf16x2c); return __builtin_bit_cast(unsigned, b); }
; __device__ __forceinline__ float sigmoidf_(float x) { return 1.f / (1.f + __expf(-x)); }
;     __device__ __forceinline__ void operator()(const f32x4 (&acc)[2][2][4][2], const Unit& u, int wr, int wc, int fr, int fq) const {
;     ...
;                     const f32x4 v0 = acc[ai][bj][m][0] + b0, v1 = acc[ai][bj][m][1] + b1; float o[8];
; #pragma unroll
;                     for (int e = 0; e < 8; ++e) { float x = (e < 4) ? v0[e & 3] : v1[e & 3];
;                         if (kind == 0) x = -0.6065306597126334f * sigmoidf_(x);
;                         else if (kind == 1) x = sigmoidf_(x);
;                         o[e] = x; }
;                     u32x4 w; w.x = cvt_pk_bf16(o[0], o[1]); w.y = cvt_pk_bf16(o[2], o[3]); w.z = cvt_pk_bf16(o[4], o[5]); w.w = cvt_pk_bf16(o[6], o[7]);
;                     *(u32x4*)(O + row * 512 + col) = w; } }
	v_pk_mul_f32 v[14:15], v[14:15], v[198:199]
	v_pk_mul_f32 v[8:9], v[8:9], v[198:199]
	v_pk_mul_f32 v[10:11], v[10:11], v[198:199]
	s_mov_b64 s[98:99], 0x28000
	v_lshl_add_u64 v[158:159], v[156:157], 0, s[98:99]
	v_cvt_pk_bf16_f32 v188, v12, v13
	v_cvt_pk_bf16_f32 v189, v14, v15
	v_cvt_pk_bf16_f32 v190, v8, v9
	v_cvt_pk_bf16_f32 v191, v10, v11
	global_store_dwordx4 v[158:159], v[188:191], off offset:256
	v_pk_add_f32 v[4:5], v[4:5], v[172:173]
	v_pk_add_f32 v[6:7], v[6:7], v[174:175]
	v_pk_add_f32 v[0:1], v[0:1], v[176:177]
	v_pk_add_f32 v[2:3], v[2:3], v[178:179]
	v_pk_mul_f32 v[4:5], v[4:5], v[196:197]
	v_pk_mul_f32 v[6:7], v[6:7], v[196:197]
	v_pk_mul_f32 v[0:1], v[0:1], v[196:197]
	v_pk_mul_f32 v[2:3], v[2:3], v[196:197]
	v_exp_f32_e32 v4, v4
	v_exp_f32_e32 v5, v5
	v_exp_f32_e32 v6, v6
	v_exp_f32_e32 v7, v7
	v_exp_f32_e32 v0, v0
	v_exp_f32_e32 v1, v1
	v_exp_f32_e32 v2, v2
	v_exp_f32_e32 v3, v3
	v_pk_add_f32 v[4:5], v[4:5], 1.0 op_sel_hi:[1,0]
	v_pk_add_f32 v[6:7], v[6:7], 1.0 op_sel_hi:[1,0]
	v_pk_add_f32 v[0:1], v[0:1], 1.0 op_sel_hi:[1,0]
	v_pk_add_f32 v[2:3], v[2:3], 1.0 op_sel_hi:[1,0]
	v_div_scale_f32 v180, s[100:101], v4, v4, 1.0
	v_rcp_f32_e32 v181, v180
	v_div_scale_f32 v182, vcc, 1.0, v4, 1.0
	v_fma_f32 v183, -v180, v181, 1.0
	v_fmac_f32_e32 v181, v183, v181
	v_mul_f32_e32 v183, v182, v181
	v_fma_f32 v184, -v180, v183, v182
	v_fmac_f32_e32 v183, v184, v181
	v_fma_f32 v180, -v180, v183, v182
	v_div_fmas_f32 v180, v180, v181, v183
	v_div_fixup_f32 v4, v180, v4, 1.0
	v_div_scale_f32 v180, s[100:101], v5, v5, 1.0
	v_rcp_f32_e32 v181, v180
	v_div_scale_f32 v182, vcc, 1.0, v5, 1.0
	v_fma_f32 v183, -v180, v181, 1.0
	v_fmac_f32_e32 v181, v183, v181
	v_mul_f32_e32 v183, v182, v181
	v_fma_f32 v184, -v180, v183, v182
	v_fmac_f32_e32 v183, v184, v181
	v_fma_f32 v180, -v180, v183, v182
	v_div_fmas_f32 v180, v180, v181, v183
	v_div_fixup_f32 v5, v180, v5, 1.0
	v_div_scale_f32 v180, s[100:101], v6, v6, 1.0
	v_rcp_f32_e32 v181, v180
	v_div_scale_f32 v182, vcc, 1.0, v6, 1.0
	v_fma_f32 v183, -v180, v181, 1.0
	v_fmac_f32_e32 v181, v183, v181
	v_mul_f32_e32 v183, v182, v181
	v_fma_f32 v184, -v180, v183, v182
	v_fmac_f32_e32 v183, v184, v181
	v_fma_f32 v180, -v180, v183, v182
	v_div_fmas_f32 v180, v180, v181, v183
	v_div_fixup_f32 v6, v180, v6, 1.0
	v_div_scale_f32 v180, s[100:101], v7, v7, 1.0
	v_rcp_f32_e32 v181, v180
	v_div_scale_f32 v182, vcc, 1.0, v7, 1.0
	v_fma_f32 v183, -v180, v181, 1.0
	v_fmac_f32_e32 v181, v183, v181
	v_mul_f32_e32 v183, v182, v181
	v_fma_f32 v184, -v180, v183, v182
	v_fmac_f32_e32 v183, v184, v181
	v_fma_f32 v180, -v180, v183, v182
	v_div_fmas_f32 v180, v180, v181, v183
	v_div_fixup_f32 v7, v180, v7, 1.0
	v_div_scale_f32 v180, s[100:101], v0, v0, 1.0
	v_rcp_f32_e32 v181, v180
	v_div_scale_f32 v182, vcc, 1.0, v0, 1.0
	v_fma_f32 v183, -v180, v181, 1.0
	v_fmac_f32_e32 v181, v183, v181
	v_mul_f32_e32 v183, v182, v181
	v_fma_f32 v184, -v180, v183, v182
	v_fmac_f32_e32 v183, v184, v181
	v_fma_f32 v180, -v180, v183, v182
	v_div_fmas_f32 v180, v180, v181, v183
	v_div_fixup_f32 v0, v180, v0, 1.0
	v_div_scale_f32 v180, s[100:101], v1, v1, 1.0
	v_rcp_f32_e32 v181, v180
	v_div_scale_f32 v182, vcc, 1.0, v1, 1.0
	v_fma_f32 v183, -v180, v181, 1.0
	v_fmac_f32_e32 v181, v183, v181
	v_mul_f32_e32 v183, v182, v181
	v_fma_f32 v184, -v180, v183, v182
	v_fmac_f32_e32 v183, v184, v181
	v_fma_f32 v180, -v180, v183, v182
	v_div_fmas_f32 v180, v180, v181, v183
	v_div_fixup_f32 v1, v180, v1, 1.0
	v_div_scale_f32 v180, s[100:101], v2, v2, 1.0
	v_rcp_f32_e32 v181, v180
	v_div_scale_f32 v182, vcc, 1.0, v2, 1.0
	v_fma_f32 v183, -v180, v181, 1.0
	v_fmac_f32_e32 v181, v183, v181
	v_mul_f32_e32 v183, v182, v181
	v_fma_f32 v184, -v180, v183, v182
	v_fmac_f32_e32 v183, v184, v181
	v_fma_f32 v180, -v180, v183, v182
	v_div_fmas_f32 v180, v180, v181, v183
	v_div_fixup_f32 v2, v180, v2, 1.0
	v_div_scale_f32 v180, s[100:101], v3, v3, 1.0
	v_rcp_f32_e32 v181, v180
	v_div_scale_f32 v182, vcc, 1.0, v3, 1.0
	v_fma_f32 v183, -v180, v181, 1.0
	v_fmac_f32_e32 v181, v183, v181
	v_mul_f32_e32 v183, v182, v181
	v_fma_f32 v184, -v180, v183, v182
	v_fmac_f32_e32 v183, v184, v181
	v_fma_f32 v180, -v180, v183, v182
	v_div_fmas_f32 v180, v180, v181, v183
	v_div_fixup_f32 v3, v180, v3, 1.0
	v_pk_mul_f32 v[4:5], v[4:5], v[198:199]
	v_pk_mul_f32 v[6:7], v[6:7], v[198:199]
	v_pk_mul_f32 v[0:1], v[0:1], v[198:199]
	v_pk_mul_f32 v[2:3], v[2:3], v[198:199]
	s_mov_b64 s[98:99], 0x2c000
	v_lshl_add_u64 v[158:159], v[156:157], 0, s[98:99]
	v_cvt_pk_bf16_f32 v192, v4, v5
	v_cvt_pk_bf16_f32 v193, v6, v7
	v_cvt_pk_bf16_f32 v194, v0, v1
	v_cvt_pk_bf16_f32 v195, v2, v3
	global_store_dwordx4 v[158:159], v[192:195], off offset:256
	s_branch .Llora_done
